# cache policy: nt also on the once-read prologue conversion and adaLN weight loads
# speedup vs baseline: 1.0045x; 1.0027x over previous
; #define LAS __attribute__((address_space(3)))
; #define LDS_WAIT() asm volatile("s_waitcnt lgkmcnt(0)" ::: "memory")
; __device__ __forceinline__ void p0_transpose_item8(const float* W, int ldw, int srccol0, int k0, unsigned char* dst, int K, LAS float* scr, int lane) {
;     { f32x4 v[8];
; #pragma unroll
;       for (int i = 0; i < 8; ++i) v[i] = *(const f32x4*)(W + (size_t)(k0 + 8 * i + (lane >> 3)) * ldw + srccol0 + 4 * (lane & 7));
; #pragma unroll
;       for (int i = 0; i < 8; ++i) { LAS float* p = scr + (8 * i + (lane >> 3)) * 33 + 4 * (lane & 7); p[0] = v[i][0]; p[1] = v[i][1]; p[2] = v[i][2]; p[3] = v[i][3]; } }
;     LDS_WAIT(); asm volatile("" ::: "memory");
;     const int c = lane & 7;
; #pragma unroll
;     for (int j = 0; j < 4; ++j) { const int n = (lane >> 3) + 8 * j; const LAS float* s = scr + (8 * c) * 33 + n;
;         u32x2 o; o.x = pk4_f8(s[0 * 33] * 32.f, s[1 * 33] * 32.f, s[2 * 33] * 32.f, s[3 * 33] * 32.f); o.y = pk4_f8(s[4 * 33] * 32.f, s[5 * 33] * 32.f, s[6 * 33] * 32.f, s[7 * 33] * 32.f);
;         *(u32x2*)(dst + (size_t)n * K + k0 + 8 * c) = o; }
;     LDS_WAIT(); asm volatile("" ::: "memory");
; __device__ __forceinline__ void p0_item(KP Pk, Frame& F, int it, LAS float* scr) {
;     unsigned char* ws = F.ws;
;     if (it < 2 * TI_L) { const int l = it / TI_L; int r = it % TI_L;
;         if (r < TI_WIN) { const int kb = r / 168, nb = r % 168, n0 = 32 * nb;
;             if (WIN_F8_L(l)) p0_transpose_item8(Pk->in[I_WIN] + (size_t)l * D * DIN, DIN, n0 < 1536 ? n0 : n0 + 32, 64 * kb, ws + WS_WIN + (size_t)l * NU * D * 2 + (size_t)n0 * D, D, scr, F.lane);
;             else p0_transpose_item(Pk->in[I_WIN] + (size_t)l * D * DIN, DIN, n0 < 1536 ? n0 : n0 + 32, 64 * kb, (bf16_t*)(ws + WS_WIN) + ((size_t)l * NU + n0) * D, D, scr, F.lane); return; }
;         r -= TI_WIN;
;         if (r < TI_WA) { if (WIN_F8_L(l)) p0_transpose_item8(Pk->in[I_WIN] + (size_t)l * D * DIN, DIN, 1536, 64 * r, ws + WS_WA + (size_t)l * 32 * D * 2, D, scr, F.lane);
.LBB0_73:
	s_add_i32 s4, s79, s80
	s_cmpk_gt_i32 s4, 0x151f
	s_cbranch_scc1 .LBB0_72
	s_mul_hi_i32 s20, s4, 0x8ca29c05
	s_add_i32 s20, s20, s4
	s_lshr_b32 s21, s20, 31
	s_ashr_i32 s20, s20, 12
	s_add_i32 s20, s20, s21
	s_mul_i32 s21, s20, 0x1d20
	s_sub_i32 s30, s4, s21
	s_cmpk_gt_i32 s30, 0x14ff
	s_mov_b64 s[22:23], -1
	s_cbranch_scc0 .LBB0_80
	s_lshl_b32 s4, s30, 6
	s_add_i32 s4, s4, 0xfffac000
	s_load_dwordx2 s[22:23], s[26:27], 0x40
	v_add_u32_e32 v1, s4, v0
	v_add_u32_e32 v26, 8, v1
	v_add_u32_e32 v28, 16, v1
	v_mad_i64_i32 v[24:25], s[28:29], v1, s53, 0
	v_mad_i64_i32 v[26:27], s[28:29], v26, s53, 0
	v_mad_i64_i32 v[28:29], s[28:29], v28, s53, 0
	s_cmp_gt_u32 s20, 1
	s_mov_b64 s[28:29], -1
	v_add_u32_e32 v35, 24, v1
	v_add_u32_e32 v34, 32, v1
	v_add_u32_e32 v33, 40, v1
	v_add_u32_e32 v32, 48, v1
	v_add_u32_e32 v1, 56, v1
	s_cbranch_scc1 .LBB0_77
	v_lshlrev_b32_e32 v76, 2, v2
	s_waitcnt lgkmcnt(0)
	v_lshl_add_u64 v[36:37], s[22:23], 0, v[76:77]
	v_lshl_add_u64 v[64:65], v[36:37], 0, s[14:15]
	v_lshl_add_u64 v[36:37], v[64:65], 0, v[24:25]
	v_lshl_add_u64 v[40:41], v[64:65], 0, v[26:27]
	v_lshl_add_u64 v[44:45], v[64:65], 0, v[28:29]
	v_mad_i64_i32 v[48:49], s[28:29], v35, s53, v[64:65]
	v_mad_i64_i32 v[52:53], s[28:29], v34, s53, v[64:65]
	v_mad_i64_i32 v[56:57], s[28:29], v33, s53, v[64:65]
	global_load_dwordx4 v[36:39], v[36:37], off nt
	s_nop 0
	global_load_dwordx4 v[40:43], v[40:41], off nt
	s_nop 0
	global_load_dwordx4 v[44:47], v[44:45], off nt
	s_nop 0
	global_load_dwordx4 v[48:51], v[48:49], off nt
	s_nop 0
	global_load_dwordx4 v[52:55], v[52:53], off nt
	s_nop 0
	global_load_dwordx4 v[56:59], v[56:57], off nt
	v_mad_i64_i32 v[60:61], s[28:29], v32, s53, v[64:65]
	global_load_dwordx4 v[60:63], v[60:61], off nt
	v_mad_i64_i32 v[64:65], s[28:29], v1, s53, v[64:65]
	global_load_dwordx4 v[64:67], v[64:65], off nt
	v_add_u32_e32 v73, v3, v30
	v_add_u32_e32 v76, 0x420, v73
	v_add_u32_e32 v78, 0x428, v73
	v_add_u32_e32 v79, 0x840, v73
	v_add_u32_e32 v84, 0x848, v73
	v_add_u32_e32 v85, 0xc60, v73
	v_add_u32_e32 v86, 0xc68, v73
	v_add_u32_e32 v87, 0x1080, v73
	v_add_u32_e32 v88, 0x1088, v73
	v_add_u32_e32 v89, 0x14a0, v73
	v_add_u32_e32 v90, 0x14a8, v73
	v_add_u32_e32 v91, 0x18c0, v73
	v_add_u32_e32 v92, 0x18c8, v73
	v_add_u32_e32 v93, 0x1ce0, v73
	v_add_u32_e32 v94, 0x1ce8, v73
	v_mov_b32_e32 v70, v77
	v_mov_b32_e32 v72, v77
	v_mov_b32_e32 v71, v77
	v_lshl_add_u64 v[68:69], v[6:7], 0, s[4:5]
	v_lshl_add_u64 v[74:75], v[68:69], 0, v[8:9]
	s_mov_b64 s[28:29], 0
	s_waitcnt vmcnt(7)
	ds_write2_b32 v73, v36, v37 offset1:1
	ds_write2_b32 v73, v38, v39 offset0:2 offset1:3
	s_waitcnt vmcnt(6)
	ds_write2_b32 v76, v40, v41 offset1:1
	ds_write2_b32 v78, v42, v43 offset1:1
	s_waitcnt vmcnt(5)
	ds_write2_b32 v79, v44, v45 offset1:1
	ds_write2_b32 v84, v46, v47 offset1:1
	s_waitcnt vmcnt(4)
	ds_write2_b32 v85, v48, v49 offset1:1
	ds_write2_b32 v86, v50, v51 offset1:1
	s_waitcnt vmcnt(3)
	ds_write2_b32 v87, v52, v53 offset1:1
	ds_write2_b32 v88, v54, v55 offset1:1
	s_waitcnt vmcnt(2)
	ds_write2_b32 v89, v56, v57 offset1:1
	ds_write2_b32 v90, v58, v59 offset1:1
	s_waitcnt vmcnt(1)
	ds_write2_b32 v91, v60, v61 offset1:1
	ds_write2_b32 v92, v62, v63 offset1:1
	s_waitcnt vmcnt(0)
	ds_write2_b32 v93, v64, v65 offset1:1
	ds_write2_b32 v94, v66, v67 offset1:1
	s_waitcnt lgkmcnt(0)
	ds_read2_b32 v[36:37], v31 offset1:8
	ds_read2_b32 v[38:39], v31 offset0:33 offset1:41
	ds_read2_b32 v[40:41], v31 offset0:66 offset1:74
	ds_read2_b32 v[42:43], v31 offset0:99 offset1:107
	ds_read2_b32 v[44:45], v31 offset0:132 offset1:140
	ds_read2_b32 v[46:47], v31 offset0:165 offset1:173
	ds_read2_b32 v[48:49], v31 offset0:198 offset1:206
	ds_read2_b32 v[50:51], v31 offset0:231 offset1:239
	s_waitcnt lgkmcnt(7)
	v_mul_f32_e32 v36, 0x42000000, v36
	s_waitcnt lgkmcnt(6)
	v_mul_f32_e32 v38, 0x42000000, v38
	v_mul_f32_e32 v37, 0x42000000, v37
	v_mul_f32_e32 v39, 0x42000000, v39
	v_med3_f32 v36, v36, s54, v81
	v_med3_f32 v38, v38, s54, v81
	s_waitcnt lgkmcnt(3)
	v_mul_f32_e32 v44, 0x42000000, v44
	s_waitcnt lgkmcnt(2)
	v_mul_f32_e32 v46, 0x42000000, v46
	v_med3_f32 v37, v37, s54, v81
	v_cvt_pk_fp8_f32 v70, v36, v38
	v_med3_f32 v36, v39, s54, v81
	v_med3_f32 v44, v44, s54, v81
	v_med3_f32 v46, v46, s54, v81
	v_cvt_pk_fp8_f32 v72, v37, v36
	v_cvt_pk_fp8_f32 v71, v44, v46
	v_mul_f32_e32 v41, 0x42000000, v41
	v_mul_f32_e32 v43, 0x42000000, v43
	v_mul_f32_e32 v40, 0x42000000, v40
	v_mul_f32_e32 v42, 0x42000000, v42
	s_waitcnt lgkmcnt(1)
	v_mul_f32_e32 v48, 0x42000000, v48
	s_waitcnt lgkmcnt(0)
	v_mul_f32_e32 v50, 0x42000000, v50
	v_mul_f32_e32 v45, 0x42000000, v45
	v_mul_f32_e32 v47, 0x42000000, v47
	v_med3_f32 v36, v41, s54, v81
	v_med3_f32 v37, v43, s54, v81
	v_med3_f32 v40, v40, s54, v81
	v_med3_f32 v42, v42, s54, v81
	v_med3_f32 v48, v48, s54, v81
	v_med3_f32 v50, v50, s54, v81
	v_cvt_pk_fp8_f32 v72, v36, v37 op_sel:[0,0,1]
	v_med3_f32 v37, v45, s54, v81
	v_med3_f32 v38, v47, s54, v81
	v_mov_b32_e32 v73, v77
	v_cvt_pk_fp8_f32 v70, v40, v42 op_sel:[0,0,1]
	v_cvt_pk_fp8_f32 v71, v48, v50 op_sel:[0,0,1]
	v_cvt_pk_fp8_f32 v73, v37, v38
	v_mul_f32_e32 v36, 0x42000000, v49
	v_mul_f32_e32 v37, 0x42000000, v51
	v_med3_f32 v36, v36, s54, v81
	v_med3_f32 v37, v37, s54, v81
	global_store_dwordx2 v[74:75], v[70:71], off
	v_cvt_pk_fp8_f32 v73, v36, v37 op_sel:[0,0,1]
	ds_read2_b32 v[38:39], v31 offset0:16 offset1:24
	ds_read2_b32 v[40:41], v31 offset0:49 offset1:57
	ds_read2_b32 v[42:43], v31 offset0:82 offset1:90
	ds_read2_b32 v[44:45], v31 offset0:115 offset1:123
	v_lshl_add_u64 v[36:37], v[68:69], 0, v[10:11]
	global_store_dwordx2 v[36:37], v[72:73], off
	s_waitcnt lgkmcnt(3)
; #define LAS __attribute__((address_space(3)))
; __device__ __forceinline__ void p0_transpose_item8(const float* W, int ldw, int srccol0, int k0, unsigned char* dst, int K, LAS float* scr, int lane) {
;     ...
;     const int c = lane & 7;
; #pragma unroll
;     for (int j = 0; j < 4; ++j) { const int n = (lane >> 3) + 8 * j; const LAS float* s = scr + (8 * c) * 33 + n;
;         u32x2 o; o.x = pk4_f8(s[0 * 33] * 32.f, s[1 * 33] * 32.f, s[2 * 33] * 32.f, s[3 * 33] * 32.f); o.y = pk4_f8(s[4 * 33] * 32.f, s[5 * 33] * 32.f, s[6 * 33] * 32.f, s[7 * 33] * 32.f);
;         *(u32x2*)(dst + (size_t)n * K + k0 + 8 * c) = o; }
	v_mul_f32_e32 v36, 0x42000000, v38
	s_waitcnt lgkmcnt(2)
	v_mul_f32_e32 v37, 0x42000000, v40
	s_waitcnt lgkmcnt(1)
	v_mul_f32_e32 v38, 0x42000000, v42
	v_med3_f32 v42, v36, s54, v81
	v_med3_f32 v37, v37, s54, v81
	v_mov_b32_e32 v36, v77
	v_cvt_pk_fp8_f32 v36, v42, v37
	ds_read2_b32 v[46:47], v31 offset0:148 offset1:156
	ds_read2_b32 v[48:49], v31 offset0:181 offset1:189
	ds_read2_b32 v[50:51], v31 offset0:214 offset1:222
	s_waitcnt lgkmcnt(3)
	v_mul_f32_e32 v40, 0x42000000, v44
	v_med3_f32 v38, v38, s54, v81
	v_med3_f32 v37, v40, s54, v81
	ds_read2_b32 v[52:53], v31 offset0:247 offset1:255
	v_cvt_pk_fp8_f32 v36, v38, v37 op_sel:[0,0,1]
	s_waitcnt lgkmcnt(3)
	v_mul_f32_e32 v37, 0x42000000, v46
	s_waitcnt lgkmcnt(2)
	v_mul_f32_e32 v38, 0x42000000, v48
	v_med3_f32 v42, v37, s54, v81
	v_med3_f32 v38, v38, s54, v81
	v_mov_b32_e32 v37, v77
	v_cvt_pk_fp8_f32 v37, v42, v38
	s_waitcnt lgkmcnt(1)
	v_mul_f32_e32 v40, 0x42000000, v50
	s_waitcnt lgkmcnt(0)
	v_mul_f32_e32 v38, 0x42000000, v52
	v_med3_f32 v40, v40, s54, v81
	v_med3_f32 v38, v38, s54, v81
	v_cvt_pk_fp8_f32 v37, v40, v38 op_sel:[0,0,1]
	v_mul_f32_e32 v38, 0x42000000, v39
	v_mul_f32_e32 v39, 0x42000000, v41
	v_med3_f32 v41, v38, s54, v81
	v_med3_f32 v39, v39, s54, v81
	v_mov_b32_e32 v38, v77
	v_cvt_pk_fp8_f32 v38, v41, v39
	v_mul_f32_e32 v40, 0x42000000, v43
	v_mul_f32_e32 v39, 0x42000000, v45
	v_med3_f32 v40, v40, s54, v81
	v_med3_f32 v39, v39, s54, v81
	v_cvt_pk_fp8_f32 v38, v40, v39 op_sel:[0,0,1]
	v_mul_f32_e32 v39, 0x42000000, v47
	v_mul_f32_e32 v40, 0x42000000, v49
	v_med3_f32 v42, v39, s54, v81
	v_med3_f32 v40, v40, s54, v81
	v_mov_b32_e32 v39, v77
	v_cvt_pk_fp8_f32 v39, v42, v40
	v_mul_f32_e32 v41, 0x42000000, v51
	v_mul_f32_e32 v40, 0x42000000, v53
	v_med3_f32 v41, v41, s54, v81
	v_med3_f32 v40, v40, s54, v81
	v_cvt_pk_fp8_f32 v39, v41, v40 op_sel:[0,0,1]
	v_lshl_add_u64 v[40:41], v[68:69], 0, v[12:13]
	global_store_dwordx2 v[40:41], v[36:37], off
	v_lshl_add_u64 v[36:37], v[68:69], 0, v[14:15]
	global_store_dwordx2 v[36:37], v[38:39], off
	s_waitcnt lgkmcnt(0)
; #define LAS __attribute__((address_space(3)))
; __device__ __forceinline__ unsigned pk2(float lo, float hi) { return f2bf(lo) | (f2bf(hi) << 16); }
; __device__ __forceinline__ unsigned pk2q(float lo, float hi) { return f2bf(q8(lo)) | (f2bf(q8(hi)) << 16); }
; #define LDS_WAIT() asm volatile("s_waitcnt lgkmcnt(0)" ::: "memory")
; __device__ __forceinline__ void p0_transpose_item(const float* W, int ldw, int srccol0, int k0, bf16_t* dst, int K, LAS float* scr, int lane, bool q = false) {
;     { f32x4 v[8];
; #pragma unroll
;       for (int i = 0; i < 8; ++i) v[i] = *(const f32x4*)(W + (size_t)(k0 + 8 * i + (lane >> 3)) * ldw + srccol0 + 4 * (lane & 7));
; #pragma unroll
;       for (int i = 0; i < 8; ++i) { LAS float* p = scr + (8 * i + (lane >> 3)) * 33 + 4 * (lane & 7); p[0] = v[i][0]; p[1] = v[i][1]; p[2] = v[i][2]; p[3] = v[i][3]; } }
;     LDS_WAIT(); asm volatile("" ::: "memory");
;     const int c = lane & 7;
; #pragma unroll
;     for (int j = 0; j < 4; ++j) { const int n = (lane >> 3) + 8 * j; const LAS float* s = scr + (8 * c) * 33 + n;
;         u32x4 o; if (q) { o.x = pk2q(s[0 * 33], s[1 * 33]); o.y = pk2q(s[2 * 33], s[3 * 33]); o.z = pk2q(s[4 * 33], s[5 * 33]); o.w = pk2q(s[6 * 33], s[7 * 33]); }
;         else { o.x = pk2(s[0 * 33], s[1 * 33]); o.y = pk2(s[2 * 33], s[3 * 33]); o.z = pk2(s[4 * 33], s[5 * 33]); o.w = pk2(s[6 * 33], s[7 * 33]); }
;         *(u32x4*)(dst + (size_t)n * K + k0 + 8 * c) = o; }
;     LDS_WAIT(); asm volatile("" ::: "memory");
; __device__ __forceinline__ void p0_item(KP Pk, Frame& F, int it, LAS float* scr) {
;     ...
;         if (r < TI_WA) { if (WIN_F8_L(l)) p0_transpose_item8(Pk->in[I_WIN] + (size_t)l * D * DIN, DIN, 1536, 64 * r, ws + WS_WA + (size_t)l * 32 * D * 2, D, scr, F.lane);
;             else p0_transpose_item(Pk->in[I_WIN] + (size_t)l * D * DIN, DIN, 1536, 64 * r, (bf16_t*)(ws + WS_WA) + (size_t)l * 32 * D, D, scr, F.lane); return; }
.LBB0_77:
	s_andn2_b64 vcc, exec, s[28:29]
	s_cbranch_vccnz .LBB0_79
	s_ashr_i32 s21, s20, 31
	s_mul_i32 s29, s20, 0x2a40000
	s_mul_hi_i32 s28, s20, 0x2a40000
	s_waitcnt lgkmcnt(0)
	s_add_u32 s22, s22, s29
	s_addc_u32 s23, s23, s28
	v_lshlrev_b32_e32 v76, 2, v2
	v_lshl_add_u64 v[36:37], s[22:23], 0, v[76:77]
	v_lshl_add_u64 v[56:57], v[36:37], 0, s[14:15]
	v_lshl_add_u64 v[24:25], v[56:57], 0, v[24:25]
	v_lshl_add_u64 v[36:37], v[56:57], 0, v[26:27]
	v_lshl_add_u64 v[28:29], v[56:57], 0, v[28:29]
	v_mad_i64_i32 v[44:45], s[22:23], v35, s53, v[56:57]
	global_load_dwordx4 v[24:27], v[24:25], off nt
	s_nop 0
	global_load_dwordx4 v[36:39], v[36:37], off nt
	s_nop 0
	global_load_dwordx4 v[40:43], v[28:29], off nt
	s_nop 0
	global_load_dwordx4 v[44:47], v[44:45], off nt
	v_mad_i64_i32 v[28:29], s[22:23], v34, s53, v[56:57]
	v_mad_i64_i32 v[34:35], s[22:23], v33, s53, v[56:57]
	global_load_dwordx4 v[48:51], v[28:29], off nt
	global_load_dwordx4 v[52:55], v[34:35], off nt
	v_mad_i64_i32 v[28:29], s[22:23], v32, s53, v[56:57]
	global_load_dwordx4 v[32:35], v[28:29], off nt
	v_mad_i64_i32 v[28:29], s[22:23], v1, s53, v[56:57]
	global_load_dwordx4 v[56:59], v[28:29], off nt
	v_add_u32_e32 v1, v3, v30
	v_add_u32_e32 v60, 0x420, v1
	v_add_u32_e32 v61, 0x428, v1
	v_add_u32_e32 v62, 0x840, v1
	v_add_u32_e32 v63, 0x848, v1
	v_add_u32_e32 v64, 0xc60, v1
	v_add_u32_e32 v65, 0xc68, v1
	v_add_u32_e32 v66, 0x1080, v1
	v_add_u32_e32 v67, 0x1088, v1
	v_add_u32_e32 v68, 0x14a0, v1
	v_add_u32_e32 v69, 0x14a8, v1
	v_add_u32_e32 v70, 0x18c0, v1
	v_add_u32_e32 v71, 0x18c8, v1
	v_add_u32_e32 v72, 0x1ce0, v1
	v_add_u32_e32 v73, 0x1ce8, v1
	s_lshl_b64 s[22:23], s[20:21], 17
	s_add_u32 s21, s12, s22
	s_addc_u32 s28, s13, s23
	s_lshl_b64 s[22:23], s[4:5], 1
	s_add_u32 s22, s21, s22
	v_lshlrev_b32_e32 v76, 1, v4
	s_addc_u32 s23, s28, s23
	v_lshl_add_u64 v[28:29], s[22:23], 0, v[76:77]
	s_waitcnt vmcnt(7)
	ds_write2_b32 v1, v24, v25 offset1:1
	ds_write2_b32 v1, v26, v27 offset0:2 offset1:3
	s_waitcnt vmcnt(6)
	ds_write2_b32 v60, v36, v37 offset1:1
	ds_write2_b32 v61, v38, v39 offset1:1
	s_waitcnt vmcnt(5)
	ds_write2_b32 v62, v40, v41 offset1:1
	ds_write2_b32 v63, v42, v43 offset1:1
	s_waitcnt vmcnt(4)
	ds_write2_b32 v64, v44, v45 offset1:1
	ds_write2_b32 v65, v46, v47 offset1:1
	s_waitcnt vmcnt(3)
	ds_write2_b32 v66, v48, v49 offset1:1
	ds_write2_b32 v67, v50, v51 offset1:1
	s_waitcnt vmcnt(2)
	ds_write2_b32 v68, v52, v53 offset1:1
	ds_write2_b32 v69, v54, v55 offset1:1
	s_waitcnt vmcnt(1)
	ds_write2_b32 v70, v32, v33 offset1:1
	ds_write2_b32 v71, v34, v35 offset1:1
	s_waitcnt vmcnt(0)
	ds_write2_b32 v72, v56, v57 offset1:1
	ds_write2_b32 v73, v58, v59 offset1:1
	s_waitcnt lgkmcnt(0)
	ds_read2_b32 v[32:33], v31 offset0:33 offset1:41
	ds_read2_b32 v[34:35], v31 offset1:8
	ds_read2_b32 v[36:37], v31 offset0:66 offset1:74
	ds_read2_b32 v[38:39], v31 offset0:99 offset1:107
	ds_read2_b32 v[40:41], v31 offset0:132 offset1:140
	ds_read2_b32 v[42:43], v31 offset0:165 offset1:173
	ds_read2_b32 v[44:45], v31 offset0:198 offset1:206
	ds_read2_b32 v[46:47], v31 offset0:231 offset1:239
	s_waitcnt lgkmcnt(5)
	v_bfe_u32 v25, v36, 16, 1
	s_waitcnt lgkmcnt(3)
	v_bfe_u32 v27, v40, 16, 1
	v_bfe_u32 v1, v34, 16, 1
	v_bfe_u32 v24, v32, 16, 1
	v_bfe_u32 v26, v38, 16, 1
	s_waitcnt lgkmcnt(2)
	v_bfe_u32 v48, v42, 16, 1
	v_add3_u32 v25, v36, v25, s55
	v_add3_u32 v27, v40, v27, s55
	s_waitcnt lgkmcnt(1)
	v_bfe_u32 v49, v44, 16, 1
	v_add3_u32 v1, v34, v1, s55
	v_add3_u32 v24, v32, v24, s55
	v_add3_u32 v26, v38, v26, s55
	v_add3_u32 v32, v42, v48, s55
	v_lshrrev_b32_e32 v25, 16, v25
	v_lshrrev_b32_e32 v27, 16, v27
	v_add3_u32 v34, v44, v49, s55
	v_lshrrev_b32_e32 v1, 16, v1
	v_and_or_b32 v25, v26, s56, v25
	v_and_or_b32 v26, v32, s56, v27
	s_waitcnt lgkmcnt(0)
	v_bfe_u32 v27, v46, 16, 1
	v_and_or_b32 v24, v24, s56, v1
	v_lshrrev_b32_e32 v1, 16, v34
	v_add3_u32 v27, v46, v27, s55
	v_and_or_b32 v27, v27, s56, v1
	v_lshl_add_u64 v[48:49], v[28:29], 0, v[16:17]
	v_bfe_u32 v1, v35, 16, 1
	global_store_dwordx4 v[48:49], v[24:27], off
	v_add3_u32 v1, v35, v1, s55
	v_lshrrev_b32_e32 v1, 16, v1
	v_bfe_u32 v24, v33, 16, 1
	v_add3_u32 v24, v33, v24, s55
	v_and_or_b32 v24, v24, s56, v1
	v_bfe_u32 v1, v37, 16, 1
	v_add3_u32 v1, v37, v1, s55
	v_bfe_u32 v25, v39, 16, 1
	v_lshrrev_b32_e32 v1, 16, v1
	v_add3_u32 v25, v39, v25, s55
	v_and_or_b32 v25, v25, s56, v1
	v_bfe_u32 v1, v41, 16, 1
	v_add3_u32 v1, v41, v1, s55
	v_bfe_u32 v26, v43, 16, 1
	v_lshrrev_b32_e32 v1, 16, v1
	v_add3_u32 v26, v43, v26, s55
	v_and_or_b32 v26, v26, s56, v1
	v_bfe_u32 v1, v45, 16, 1
	v_add3_u32 v1, v45, v1, s55
	v_bfe_u32 v27, v47, 16, 1
	v_lshrrev_b32_e32 v1, 16, v1
	v_add3_u32 v27, v47, v27, s55
	ds_read2_b32 v[32:33], v31 offset0:16 offset1:24
	v_and_or_b32 v27, v27, s56, v1
	v_lshl_add_u64 v[34:35], v[28:29], 0, v[18:19]
	global_store_dwordx4 v[34:35], v[24:27], off
	ds_read2_b32 v[34:35], v31 offset0:49 offset1:57
	ds_read2_b32 v[36:37], v31 offset0:82 offset1:90
	ds_read2_b32 v[38:39], v31 offset0:115 offset1:123
	s_waitcnt lgkmcnt(3)
	v_bfe_u32 v1, v32, 16, 1
	v_add3_u32 v1, v32, v1, s55
	s_waitcnt lgkmcnt(2)
	v_bfe_u32 v24, v34, 16, 1
	ds_read2_b32 v[40:41], v31 offset0:148 offset1:156
	v_lshrrev_b32_e32 v1, 16, v1
	v_add3_u32 v24, v34, v24, s55
	ds_read2_b32 v[42:43], v31 offset0:181 offset1:189
	v_and_or_b32 v24, v24, s56, v1
	s_waitcnt lgkmcnt(3)
	v_bfe_u32 v1, v36, 16, 1
	v_add3_u32 v1, v36, v1, s55
	s_waitcnt lgkmcnt(2)
	v_bfe_u32 v25, v38, 16, 1
	ds_read2_b32 v[44:45], v31 offset0:214 offset1:222
	v_lshrrev_b32_e32 v1, 16, v1
	v_add3_u32 v25, v38, v25, s55
	ds_read2_b32 v[46:47], v31 offset0:247 offset1:255
	v_and_or_b32 v25, v25, s56, v1
	s_waitcnt lgkmcnt(3)
	v_bfe_u32 v1, v40, 16, 1
	v_add3_u32 v1, v40, v1, s55
	s_waitcnt lgkmcnt(2)
	v_bfe_u32 v26, v42, 16, 1
	v_lshrrev_b32_e32 v1, 16, v1
	v_add3_u32 v26, v42, v26, s55
	v_and_or_b32 v26, v26, s56, v1
	s_waitcnt lgkmcnt(1)
	v_bfe_u32 v1, v44, 16, 1
	v_add3_u32 v1, v44, v1, s55
	s_waitcnt lgkmcnt(0)
	v_bfe_u32 v27, v46, 16, 1
	v_lshrrev_b32_e32 v1, 16, v1
	v_add3_u32 v27, v46, v27, s55
	v_and_or_b32 v27, v27, s56, v1
	v_lshl_add_u64 v[48:49], v[28:29], 0, v[20:21]
	v_bfe_u32 v1, v33, 16, 1
	global_store_dwordx4 v[48:49], v[24:27], off
	v_add3_u32 v1, v33, v1, s55
	v_lshrrev_b32_e32 v1, 16, v1
	v_bfe_u32 v24, v35, 16, 1
	v_add3_u32 v24, v35, v24, s55
	v_and_or_b32 v24, v24, s56, v1
	v_bfe_u32 v1, v37, 16, 1
	v_add3_u32 v1, v37, v1, s55
	v_bfe_u32 v25, v39, 16, 1
	v_lshrrev_b32_e32 v1, 16, v1
	v_add3_u32 v25, v39, v25, s55
	v_and_or_b32 v25, v25, s56, v1
	v_bfe_u32 v1, v41, 16, 1
	v_add3_u32 v1, v41, v1, s55
	v_bfe_u32 v26, v43, 16, 1
	v_lshrrev_b32_e32 v1, 16, v1
	v_add3_u32 v26, v43, v26, s55
	v_and_or_b32 v26, v26, s56, v1
	v_bfe_u32 v1, v45, 16, 1
	v_add3_u32 v1, v45, v1, s55
	v_bfe_u32 v27, v47, 16, 1
	v_lshrrev_b32_e32 v1, 16, v1
	v_add3_u32 v27, v47, v27, s55
	v_and_or_b32 v27, v27, s56, v1
	v_lshl_add_u64 v[28:29], v[28:29], 0, v[22:23]
	global_store_dwordx4 v[28:29], v[24:27], off
	s_waitcnt lgkmcnt(0)

; #define LAS __attribute__((address_space(3)))
; #define LDS_WAIT() asm volatile("s_waitcnt lgkmcnt(0)" ::: "memory")
; __device__ __forceinline__ void p0_transpose_item8(const float* W, int ldw, int srccol0, int k0, unsigned char* dst, int K, LAS float* scr, int lane) {
;     { f32x4 v[8];
; #pragma unroll
;       for (int i = 0; i < 8; ++i) v[i] = *(const f32x4*)(W + (size_t)(k0 + 8 * i + (lane >> 3)) * ldw + srccol0 + 4 * (lane & 7));
; #pragma unroll
;       for (int i = 0; i < 8; ++i) { LAS float* p = scr + (8 * i + (lane >> 3)) * 33 + 4 * (lane & 7); p[0] = v[i][0]; p[1] = v[i][1]; p[2] = v[i][2]; p[3] = v[i][3]; } }
;     LDS_WAIT(); asm volatile("" ::: "memory");
;     const int c = lane & 7;
; #pragma unroll
;     for (int j = 0; j < 4; ++j) { const int n = (lane >> 3) + 8 * j; const LAS float* s = scr + (8 * c) * 33 + n;
;         u32x2 o; o.x = pk4_f8(s[0 * 33] * 32.f, s[1 * 33] * 32.f, s[2 * 33] * 32.f, s[3 * 33] * 32.f); o.y = pk4_f8(s[4 * 33] * 32.f, s[5 * 33] * 32.f, s[6 * 33] * 32.f, s[7 * 33] * 32.f);
;         *(u32x2*)(dst + (size_t)n * K + k0 + 8 * c) = o; }
;     LDS_WAIT(); asm volatile("" ::: "memory");
; __device__ __forceinline__ void p0_item(KP Pk, Frame& F, int it, LAS float* scr) {
;     ...
;     if (it < 2 * TI_L) { const int l = it / TI_L; int r = it % TI_L;
;         if (r < TI_WIN) { const int kb = r / 168, nb = r % 168, n0 = 32 * nb;
;             if (WIN_F8_L(l)) p0_transpose_item8(Pk->in[I_WIN] + (size_t)l * D * DIN, DIN, n0 < 1536 ? n0 : n0 + 32, 64 * kb, ws + WS_WIN + (size_t)l * NU * D * 2 + (size_t)n0 * D, D, scr, F.lane);
.LBB0_80:
	s_andn2_b64 vcc, exec, s[22:23]
	s_cbranch_vccnz .LBB0_72
	s_mul_i32 s4, s30, 0xffffc30d
	s_lshr_b32 s4, s4, 16
	s_add_i32 s4, s4, s30
	s_sext_i32_i16 s21, s4
	s_ashr_i32 s21, s21, 7
	s_bfe_u32 s4, s4, 0x1000f
	s_add_i32 s4, s21, s4
	s_sext_i32_i16 s21, s4
	s_mulk_i32 s4, 0xa8
	s_sub_i32 s4, s30, s4
	s_sext_i32_i16 s4, s4
	s_lshl_b32 s30, s4, 5
	s_add_i32 s22, s30, 32
	s_cmp_lt_i32 s4, 48
	s_cselect_b32 s28, s30, s22
	s_lshl_b32 s22, s21, 6
	s_waitcnt lgkmcnt(0)
	s_load_dwordx2 s[34:35], s[26:27], 0x40
	v_add_u32_e32 v1, s22, v0
	v_add_u32_e32 v26, 8, v1
	s_ashr_i32 s29, s28, 31
	v_mad_i64_i32 v[24:25], s[36:37], v1, s53, 0
	v_mad_i64_i32 v[26:27], s[36:37], v26, s53, 0
	v_add_u32_e32 v49, 16, v1
	v_add_u32_e32 v48, 24, v1
	v_add_u32_e32 v47, 32, v1
	v_add_u32_e32 v46, 40, v1
	v_add_u32_e32 v45, 48, v1
	v_add_u32_e32 v44, 56, v1
	v_add_u32_e32 v1, v3, v30
	s_cmp_gt_u32 s20, 1
	s_mov_b64 s[36:37], -1
	v_lshlrev_b32_e32 v76, 2, v2
	v_add_u32_e32 v28, 0x420, v1
	v_add_u32_e32 v29, 0x428, v1
	v_add_u32_e32 v32, 0x840, v1
	v_add_u32_e32 v33, 0x848, v1
	v_add_u32_e32 v34, 0xc60, v1
	v_add_u32_e32 v35, 0xc68, v1
	v_add_u32_e32 v36, 0x1080, v1
	v_add_u32_e32 v37, 0x1088, v1
	v_add_u32_e32 v38, 0x14a0, v1
	v_add_u32_e32 v39, 0x14a8, v1
	v_add_u32_e32 v40, 0x18c0, v1
	v_add_u32_e32 v41, 0x18c8, v1
	v_add_u32_e32 v42, 0x1ce0, v1
	v_add_u32_e32 v43, 0x1ce8, v1
	s_cbranch_scc1 .LBB0_83
	s_ashr_i32 s31, s30, 31
	s_lshl_b64 s[36:37], s[30:31], 11
	s_add_u32 s4, s39, s36
	s_addc_u32 s21, s40, s37
	s_lshl_b64 s[36:37], s[28:29], 2
	s_waitcnt lgkmcnt(0)
	s_add_u32 s36, s34, s36
	s_addc_u32 s37, s35, s37
	v_lshl_add_u64 v[74:75], s[36:37], 0, v[76:77]
	v_lshl_add_u64 v[50:51], v[74:75], 0, v[24:25]
	v_lshl_add_u64 v[54:55], v[74:75], 0, v[26:27]
	v_mad_i64_i32 v[58:59], s[36:37], v49, s53, v[74:75]
	v_mad_i64_i32 v[62:63], s[36:37], v48, s53, v[74:75]
	v_mad_i64_i32 v[66:67], s[36:37], v47, s53, v[74:75]
	v_mad_i64_i32 v[70:71], s[36:37], v46, s53, v[74:75]
	global_load_dwordx4 v[50:53], v[50:51], off nt
	s_nop 0
	global_load_dwordx4 v[54:57], v[54:55], off nt
	s_nop 0
	global_load_dwordx4 v[58:61], v[58:59], off nt
	s_nop 0
	global_load_dwordx4 v[62:65], v[62:63], off nt
	s_nop 0
	global_load_dwordx4 v[66:69], v[66:67], off nt
	s_nop 0
	global_load_dwordx4 v[70:73], v[70:71], off nt
	v_mad_i64_i32 v[78:79], s[36:37], v45, s53, v[74:75]
	global_load_dwordx4 v[84:87], v[78:79], off nt
	v_mad_i64_i32 v[74:75], s[36:37], v44, s53, v[74:75]
	global_load_dwordx4 v[88:91], v[74:75], off nt
	v_mov_b32_e32 v74, v77
	v_mov_b32_e32 v75, v77
	s_ashr_i32 s23, s22, 31
	v_mov_b32_e32 v78, v77
	v_mov_b32_e32 v79, v77
	s_add_u32 s36, s4, s22
	s_addc_u32 s37, s21, s23
	v_lshl_add_u64 v[92:93], s[36:37], 0, v[4:5]
	v_lshl_add_u64 v[94:95], v[92:93], 0, v[8:9]
	v_lshl_add_u64 v[96:97], v[92:93], 0, v[10:11]
	s_mov_b64 s[36:37], 0
	s_waitcnt vmcnt(7)
	ds_write2_b32 v1, v50, v51 offset1:1
	ds_write2_b32 v1, v52, v53 offset0:2 offset1:3
	s_waitcnt vmcnt(6)
	ds_write2_b32 v28, v54, v55 offset1:1
	ds_write2_b32 v29, v56, v57 offset1:1
	s_waitcnt vmcnt(5)
	ds_write2_b32 v32, v58, v59 offset1:1
	ds_write2_b32 v33, v60, v61 offset1:1
	s_waitcnt vmcnt(4)
	ds_write2_b32 v34, v62, v63 offset1:1
	ds_write2_b32 v35, v64, v65 offset1:1
	s_waitcnt vmcnt(3)
	ds_write2_b32 v36, v66, v67 offset1:1
	ds_write2_b32 v37, v68, v69 offset1:1
	s_waitcnt vmcnt(2)
	ds_write2_b32 v38, v70, v71 offset1:1
	ds_write2_b32 v39, v72, v73 offset1:1
	s_waitcnt vmcnt(1)
	ds_write2_b32 v40, v84, v85 offset1:1
	ds_write2_b32 v41, v86, v87 offset1:1
	s_waitcnt vmcnt(0)
	ds_write2_b32 v42, v88, v89 offset1:1
	ds_write2_b32 v43, v90, v91 offset1:1
	s_waitcnt lgkmcnt(0)
	ds_read2_b32 v[50:51], v31 offset1:8
	ds_read2_b32 v[52:53], v31 offset0:33 offset1:41
	ds_read2_b32 v[54:55], v31 offset0:66 offset1:74
	ds_read2_b32 v[56:57], v31 offset0:99 offset1:107
	ds_read2_b32 v[58:59], v31 offset0:132 offset1:140
	ds_read2_b32 v[60:61], v31 offset0:165 offset1:173
	ds_read2_b32 v[62:63], v31 offset0:198 offset1:206
	ds_read2_b32 v[64:65], v31 offset0:231 offset1:239
	s_waitcnt lgkmcnt(7)
	v_mul_f32_e32 v50, 0x42000000, v50
	s_waitcnt lgkmcnt(6)
	v_mul_f32_e32 v52, 0x42000000, v52
	s_waitcnt lgkmcnt(3)
	v_mul_f32_e32 v58, 0x42000000, v58
	s_waitcnt lgkmcnt(2)
	v_mul_f32_e32 v60, 0x42000000, v60
	v_med3_f32 v50, v50, s54, v81
	v_med3_f32 v52, v52, s54, v81
	v_med3_f32 v58, v58, s54, v81
	v_med3_f32 v60, v60, s54, v81
	v_cvt_pk_fp8_f32 v74, v50, v52
	v_cvt_pk_fp8_f32 v75, v58, v60
	v_mul_f32_e32 v54, 0x42000000, v54
	v_mul_f32_e32 v56, 0x42000000, v56
	s_waitcnt lgkmcnt(1)
	v_mul_f32_e32 v62, 0x42000000, v62
	s_waitcnt lgkmcnt(0)
	v_mul_f32_e32 v64, 0x42000000, v64
	v_mul_f32_e32 v51, 0x42000000, v51
	v_mul_f32_e32 v53, 0x42000000, v53
	v_mul_f32_e32 v59, 0x42000000, v59
	v_mul_f32_e32 v61, 0x42000000, v61
	v_med3_f32 v54, v54, s54, v81
	v_med3_f32 v56, v56, s54, v81
	v_med3_f32 v62, v62, s54, v81
	v_med3_f32 v64, v64, s54, v81
	v_med3_f32 v51, v51, s54, v81
	v_med3_f32 v53, v53, s54, v81
	v_med3_f32 v59, v59, s54, v81
	v_med3_f32 v61, v61, s54, v81
	v_cvt_pk_fp8_f32 v74, v54, v56 op_sel:[0,0,1]
	v_cvt_pk_fp8_f32 v75, v62, v64 op_sel:[0,0,1]
	v_cvt_pk_fp8_f32 v78, v51, v53
	v_cvt_pk_fp8_f32 v79, v59, v61
	v_mul_f32_e32 v55, 0x42000000, v55
	v_mul_f32_e32 v57, 0x42000000, v57
	v_mul_f32_e32 v63, 0x42000000, v63
	v_mul_f32_e32 v65, 0x42000000, v65
	v_med3_f32 v55, v55, s54, v81
	v_med3_f32 v57, v57, s54, v81
	v_med3_f32 v63, v63, s54, v81
	v_med3_f32 v50, v65, s54, v81
	global_store_dwordx2 v[94:95], v[74:75], off
	v_cvt_pk_fp8_f32 v78, v55, v57 op_sel:[0,0,1]
	v_cvt_pk_fp8_f32 v79, v63, v50 op_sel:[0,0,1]
	ds_read2_b32 v[50:51], v31 offset0:16 offset1:24
	ds_read2_b32 v[52:53], v31 offset0:49 offset1:57
	ds_read2_b32 v[54:55], v31 offset0:82 offset1:90
	ds_read2_b32 v[56:57], v31 offset0:115 offset1:123
	v_mov_b32_e32 v58, v77
	s_waitcnt lgkmcnt(3)
; #define LAS __attribute__((address_space(3)))
; __device__ __forceinline__ void p0_transpose_item8(const float* W, int ldw, int srccol0, int k0, unsigned char* dst, int K, LAS float* scr, int lane) {
;     ...
;     const int c = lane & 7;
; #pragma unroll
;     for (int j = 0; j < 4; ++j) { const int n = (lane >> 3) + 8 * j; const LAS float* s = scr + (8 * c) * 33 + n;
;         u32x2 o; o.x = pk4_f8(s[0 * 33] * 32.f, s[1 * 33] * 32.f, s[2 * 33] * 32.f, s[3 * 33] * 32.f); o.y = pk4_f8(s[4 * 33] * 32.f, s[5 * 33] * 32.f, s[6 * 33] * 32.f, s[7 * 33] * 32.f);
;         *(u32x2*)(dst + (size_t)n * K + k0 + 8 * c) = o; }
	v_mul_f32_e32 v50, 0x42000000, v50
	s_waitcnt lgkmcnt(2)
	v_mul_f32_e32 v52, 0x42000000, v52
	global_store_dwordx2 v[96:97], v[78:79], off
	v_med3_f32 v50, v50, s54, v81
	v_med3_f32 v52, v52, s54, v81
	v_cvt_pk_fp8_f32 v58, v50, v52
	ds_read2_b32 v[60:61], v31 offset0:148 offset1:156
	ds_read2_b32 v[62:63], v31 offset0:181 offset1:189
	ds_read2_b32 v[64:65], v31 offset0:214 offset1:222
	s_waitcnt lgkmcnt(4)
	v_mul_f32_e32 v54, 0x42000000, v54
	s_waitcnt lgkmcnt(3)
	v_mul_f32_e32 v56, 0x42000000, v56
	v_med3_f32 v54, v54, s54, v81
	v_med3_f32 v50, v56, s54, v81
	ds_read2_b32 v[66:67], v31 offset0:247 offset1:255
	v_cvt_pk_fp8_f32 v58, v54, v50 op_sel:[0,0,1]
	s_waitcnt lgkmcnt(3)
	v_mul_f32_e32 v50, 0x42000000, v60
	s_waitcnt lgkmcnt(2)
	v_mul_f32_e32 v52, 0x42000000, v62
	v_med3_f32 v50, v50, s54, v81
	v_med3_f32 v52, v52, s54, v81
	v_mov_b32_e32 v59, v77
	v_cvt_pk_fp8_f32 v59, v50, v52
	s_waitcnt lgkmcnt(1)
	v_mul_f32_e32 v54, 0x42000000, v64
	s_waitcnt lgkmcnt(0)
	v_mul_f32_e32 v50, 0x42000000, v66
	v_med3_f32 v52, v54, s54, v81
	v_med3_f32 v50, v50, s54, v81
	v_cvt_pk_fp8_f32 v59, v52, v50 op_sel:[0,0,1]
	v_mul_f32_e32 v50, 0x42000000, v51
	v_mul_f32_e32 v51, 0x42000000, v53
	v_med3_f32 v53, v50, s54, v81
	v_med3_f32 v51, v51, s54, v81
	v_mov_b32_e32 v50, v77
	v_cvt_pk_fp8_f32 v50, v53, v51
	v_mul_f32_e32 v52, 0x42000000, v55
	v_mul_f32_e32 v51, 0x42000000, v57
	v_med3_f32 v52, v52, s54, v81
	v_med3_f32 v51, v51, s54, v81
	v_cvt_pk_fp8_f32 v50, v52, v51 op_sel:[0,0,1]
	v_mul_f32_e32 v51, 0x42000000, v61
	v_mul_f32_e32 v52, 0x42000000, v63
	v_med3_f32 v54, v51, s54, v81
	v_med3_f32 v52, v52, s54, v81
	v_mov_b32_e32 v51, v77
	v_cvt_pk_fp8_f32 v51, v54, v52
	v_mul_f32_e32 v53, 0x42000000, v65
	v_mul_f32_e32 v52, 0x42000000, v67
	v_med3_f32 v53, v53, s54, v81
	v_med3_f32 v52, v52, s54, v81
	v_cvt_pk_fp8_f32 v51, v53, v52 op_sel:[0,0,1]
	v_lshl_add_u64 v[52:53], v[92:93], 0, v[12:13]
	global_store_dwordx2 v[52:53], v[58:59], off
	v_lshl_add_u64 v[52:53], v[92:93], 0, v[14:15]
	global_store_dwordx2 v[52:53], v[50:51], off
	s_waitcnt lgkmcnt(0)
; #define LAS __attribute__((address_space(3)))
; __device__ __forceinline__ unsigned pk2(float lo, float hi) { return f2bf(lo) | (f2bf(hi) << 16); }
; __device__ __forceinline__ unsigned pk2q(float lo, float hi) { return f2bf(q8(lo)) | (f2bf(q8(hi)) << 16); }
; #define LDS_WAIT() asm volatile("s_waitcnt lgkmcnt(0)" ::: "memory")
; __device__ __forceinline__ void p0_transpose_item(const float* W, int ldw, int srccol0, int k0, bf16_t* dst, int K, LAS float* scr, int lane, bool q = false) {
;     { f32x4 v[8];
; #pragma unroll
;       for (int i = 0; i < 8; ++i) v[i] = *(const f32x4*)(W + (size_t)(k0 + 8 * i + (lane >> 3)) * ldw + srccol0 + 4 * (lane & 7));
; #pragma unroll
;       for (int i = 0; i < 8; ++i) { LAS float* p = scr + (8 * i + (lane >> 3)) * 33 + 4 * (lane & 7); p[0] = v[i][0]; p[1] = v[i][1]; p[2] = v[i][2]; p[3] = v[i][3]; } }
;     LDS_WAIT(); asm volatile("" ::: "memory");
;     const int c = lane & 7;
; #pragma unroll
;     for (int j = 0; j < 4; ++j) { const int n = (lane >> 3) + 8 * j; const LAS float* s = scr + (8 * c) * 33 + n;
;         u32x4 o; if (q) { o.x = pk2q(s[0 * 33], s[1 * 33]); o.y = pk2q(s[2 * 33], s[3 * 33]); o.z = pk2q(s[4 * 33], s[5 * 33]); o.w = pk2q(s[6 * 33], s[7 * 33]); }
;         else { o.x = pk2(s[0 * 33], s[1 * 33]); o.y = pk2(s[2 * 33], s[3 * 33]); o.z = pk2(s[4 * 33], s[5 * 33]); o.w = pk2(s[6 * 33], s[7 * 33]); }
;         *(u32x4*)(dst + (size_t)n * K + k0 + 8 * c) = o; }
;     LDS_WAIT(); asm volatile("" ::: "memory");
; __device__ __forceinline__ void p0_item(KP Pk, Frame& F, int it, LAS float* scr) {
;     ...
;             else p0_transpose_item(Pk->in[I_WIN] + (size_t)l * D * DIN, DIN, n0 < 1536 ? n0 : n0 + 32, 64 * kb, (bf16_t*)(ws + WS_WIN) + ((size_t)l * NU + n0) * D, D, scr, F.lane); return; }
.LBB0_83:
	s_andn2_b64 vcc, exec, s[36:37]
	s_cbranch_vccnz .LBB0_72
	s_mul_i32 s21, s20, 0x2a40000
	s_mul_hi_i32 s4, s20, 0x2a40000
	s_waitcnt lgkmcnt(0)
	s_add_u32 s23, s34, s21
	s_addc_u32 s4, s35, s4
	s_mul_hi_i32 s21, s20, 0x1500
	s_mulk_i32 s20, 0x1500
	s_ashr_i32 s31, s30, 31
	s_add_u32 s20, s20, s30
	s_addc_u32 s21, s21, s31
	s_lshl_b64 s[20:21], s[20:21], 12
	s_add_u32 s30, s39, s20
	s_addc_u32 s31, s40, s21
	s_lshl_b64 s[20:21], s[28:29], 2
	s_add_u32 s20, s23, s20
	s_addc_u32 s21, s4, s21
	v_lshl_add_u64 v[70:71], s[20:21], 0, v[76:77]
	v_lshl_add_u64 v[24:25], v[70:71], 0, v[24:25]
	v_lshl_add_u64 v[50:51], v[70:71], 0, v[26:27]
	v_mad_i64_i32 v[54:55], s[20:21], v49, s53, v[70:71]
	v_mad_i64_i32 v[48:49], s[20:21], v48, s53, v[70:71]
	global_load_dwordx4 v[24:27], v[24:25], off nt
	s_nop 0
	global_load_dwordx4 v[50:53], v[50:51], off nt
	s_nop 0
	global_load_dwordx4 v[54:57], v[54:55], off nt
	s_nop 0
	global_load_dwordx4 v[58:61], v[48:49], off nt
	v_mad_i64_i32 v[48:49], s[20:21], v47, s53, v[70:71]
	v_mad_i64_i32 v[62:63], s[20:21], v46, s53, v[70:71]
	global_load_dwordx4 v[46:49], v[48:49], off nt
	s_nop 0
	global_load_dwordx4 v[62:65], v[62:63], off nt
	v_mad_i64_i32 v[66:67], s[20:21], v45, s53, v[70:71]
	global_load_dwordx4 v[66:69], v[66:67], off nt
	v_mad_i64_i32 v[44:45], s[20:21], v44, s53, v[70:71]
	global_load_dwordx4 v[70:73], v[44:45], off nt
	s_ashr_i32 s23, s22, 31
	s_lshl_b64 s[20:21], s[22:23], 1
	s_add_u32 s20, s30, s20
	v_lshlrev_b32_e32 v76, 1, v4
	s_addc_u32 s21, s31, s21
	v_lshl_add_u64 v[44:45], s[20:21], 0, v[76:77]
	v_lshl_add_u64 v[74:75], v[44:45], 0, v[16:17]
	s_waitcnt vmcnt(7)
	ds_write2_b32 v1, v24, v25 offset1:1
	ds_write2_b32 v1, v26, v27 offset0:2 offset1:3
	s_waitcnt vmcnt(6)
	ds_write2_b32 v28, v50, v51 offset1:1
	ds_write2_b32 v29, v52, v53 offset1:1
	s_waitcnt vmcnt(5)
	ds_write2_b32 v32, v54, v55 offset1:1
	ds_write2_b32 v33, v56, v57 offset1:1
	s_waitcnt vmcnt(4)
	ds_write2_b32 v34, v58, v59 offset1:1
	ds_write2_b32 v35, v60, v61 offset1:1
	s_waitcnt vmcnt(3)
	ds_write2_b32 v36, v46, v47 offset1:1
	ds_write2_b32 v37, v48, v49 offset1:1
	s_waitcnt vmcnt(2)
	ds_write2_b32 v38, v62, v63 offset1:1
	ds_write2_b32 v39, v64, v65 offset1:1
	s_waitcnt vmcnt(1)
	ds_write2_b32 v40, v66, v67 offset1:1
	ds_write2_b32 v41, v68, v69 offset1:1
	s_waitcnt vmcnt(0)
	ds_write2_b32 v42, v70, v71 offset1:1
	ds_write2_b32 v43, v72, v73 offset1:1
	s_waitcnt lgkmcnt(0)
	ds_read2_b32 v[24:25], v31 offset0:33 offset1:41
	ds_read2_b32 v[26:27], v31 offset1:8
	ds_read2_b32 v[28:29], v31 offset0:66 offset1:74
	ds_read2_b32 v[32:33], v31 offset0:99 offset1:107
	ds_read2_b32 v[34:35], v31 offset0:132 offset1:140
	ds_read2_b32 v[36:37], v31 offset0:165 offset1:173
	ds_read2_b32 v[38:39], v31 offset0:198 offset1:206
	ds_read2_b32 v[40:41], v31 offset0:231 offset1:239
	s_waitcnt lgkmcnt(6)
	v_bfe_u32 v1, v26, 16, 1
	v_bfe_u32 v42, v24, 16, 1
	v_add3_u32 v1, v26, v1, s55
	s_waitcnt lgkmcnt(5)
	v_bfe_u32 v43, v28, 16, 1
	s_waitcnt lgkmcnt(4)
	v_bfe_u32 v46, v32, 16, 1
	s_waitcnt lgkmcnt(3)
	v_bfe_u32 v47, v34, 16, 1
	s_waitcnt lgkmcnt(2)
	v_bfe_u32 v48, v36, 16, 1
	s_waitcnt lgkmcnt(1)
	v_bfe_u32 v49, v38, 16, 1
	s_waitcnt lgkmcnt(0)
	v_bfe_u32 v50, v40, 16, 1
	v_bfe_u32 v52, v25, 16, 1
	v_bfe_u32 v53, v29, 16, 1
	v_add3_u32 v24, v24, v42, s55
	v_lshrrev_b32_e32 v1, 16, v1
	v_bfe_u32 v51, v27, 16, 1
	v_add3_u32 v26, v28, v43, s55
	v_add3_u32 v28, v32, v46, s55
	v_add3_u32 v32, v34, v47, s55
	v_add3_u32 v34, v36, v48, s55
	v_add3_u32 v36, v38, v49, s55
	v_add3_u32 v38, v40, v50, s55
	v_add3_u32 v40, v25, v52, s55
	v_add3_u32 v25, v29, v53, s55
	v_and_or_b32 v24, v24, s56, v1
	v_bfe_u32 v1, v33, 16, 1
	v_add3_u32 v27, v27, v51, s55
	v_lshrrev_b32_e32 v26, 16, v26
	v_lshrrev_b32_e32 v29, 16, v32
	v_lshrrev_b32_e32 v32, 16, v36
	v_lshrrev_b32_e32 v42, 16, v25
	v_add3_u32 v1, v33, v1, s55
	v_lshrrev_b32_e32 v36, 16, v27
	v_and_or_b32 v25, v28, s56, v26
	v_and_or_b32 v26, v34, s56, v29
	v_and_or_b32 v27, v38, s56, v32
	v_and_or_b32 v33, v1, s56, v42
	v_bfe_u32 v1, v35, 16, 1
	global_store_dwordx4 v[74:75], v[24:27], off
	v_add3_u32 v1, v35, v1, s55
	v_lshrrev_b32_e32 v1, 16, v1
	v_bfe_u32 v24, v37, 16, 1
	v_add3_u32 v24, v37, v24, s55
	v_and_or_b32 v34, v24, s56, v1
	v_bfe_u32 v1, v39, 16, 1
	v_add3_u32 v1, v39, v1, s55
	v_bfe_u32 v24, v41, 16, 1
	v_lshrrev_b32_e32 v1, 16, v1
	v_add3_u32 v24, v41, v24, s55
	v_and_or_b32 v32, v40, s56, v36
	ds_read2_b32 v[28:29], v31 offset0:16 offset1:24
	v_and_or_b32 v35, v24, s56, v1
	v_lshl_add_u64 v[24:25], v[44:45], 0, v[18:19]
	global_store_dwordx4 v[24:25], v[32:35], off
	ds_read2_b32 v[32:33], v31 offset0:49 offset1:57
	ds_read2_b32 v[34:35], v31 offset0:82 offset1:90
	ds_read2_b32 v[36:37], v31 offset0:115 offset1:123
	s_waitcnt lgkmcnt(3)
	v_bfe_u32 v1, v28, 16, 1
	v_add3_u32 v1, v28, v1, s55
	s_waitcnt lgkmcnt(2)
	v_bfe_u32 v24, v32, 16, 1
	ds_read2_b32 v[38:39], v31 offset0:148 offset1:156
	v_lshrrev_b32_e32 v1, 16, v1
	v_add3_u32 v24, v32, v24, s55
	ds_read2_b32 v[40:41], v31 offset0:181 offset1:189
	v_and_or_b32 v24, v24, s56, v1
	s_waitcnt lgkmcnt(3)
	v_bfe_u32 v1, v34, 16, 1
	v_add3_u32 v1, v34, v1, s55
	s_waitcnt lgkmcnt(2)
	v_bfe_u32 v25, v36, 16, 1
	ds_read2_b32 v[42:43], v31 offset0:214 offset1:222
	v_lshrrev_b32_e32 v1, 16, v1
	v_add3_u32 v25, v36, v25, s55
	ds_read2_b32 v[46:47], v31 offset0:247 offset1:255
	v_and_or_b32 v25, v25, s56, v1
	s_waitcnt lgkmcnt(3)
	v_bfe_u32 v1, v38, 16, 1
	v_add3_u32 v1, v38, v1, s55
	s_waitcnt lgkmcnt(2)
	v_bfe_u32 v26, v40, 16, 1
	v_lshrrev_b32_e32 v1, 16, v1
	v_add3_u32 v26, v40, v26, s55
	v_and_or_b32 v26, v26, s56, v1
	s_waitcnt lgkmcnt(1)
	v_bfe_u32 v1, v42, 16, 1
	v_add3_u32 v1, v42, v1, s55
	s_waitcnt lgkmcnt(0)
	v_bfe_u32 v27, v46, 16, 1
	v_lshrrev_b32_e32 v1, 16, v1
	v_add3_u32 v27, v46, v27, s55
	v_and_or_b32 v27, v27, s56, v1
	v_lshl_add_u64 v[48:49], v[44:45], 0, v[20:21]
	v_bfe_u32 v1, v29, 16, 1
	global_store_dwordx4 v[48:49], v[24:27], off
	v_add3_u32 v1, v29, v1, s55
	v_lshrrev_b32_e32 v1, 16, v1
	v_bfe_u32 v24, v33, 16, 1
	v_add3_u32 v24, v33, v24, s55
	v_and_or_b32 v24, v24, s56, v1
	v_bfe_u32 v1, v35, 16, 1
	v_add3_u32 v1, v35, v1, s55
	v_bfe_u32 v25, v37, 16, 1
	v_lshrrev_b32_e32 v1, 16, v1
	v_add3_u32 v25, v37, v25, s55
	v_and_or_b32 v25, v25, s56, v1
	v_bfe_u32 v1, v39, 16, 1
	v_add3_u32 v1, v39, v1, s55
	v_bfe_u32 v26, v41, 16, 1
	v_lshrrev_b32_e32 v1, 16, v1
	v_add3_u32 v26, v41, v26, s55
	v_and_or_b32 v26, v26, s56, v1
	v_bfe_u32 v1, v43, 16, 1
	v_add3_u32 v1, v43, v1, s55
	v_bfe_u32 v27, v47, 16, 1
	v_lshrrev_b32_e32 v1, 16, v1
	v_add3_u32 v27, v47, v27, s55
	v_and_or_b32 v27, v27, s56, v1
	v_lshl_add_u64 v[28:29], v[44:45], 0, v[22:23]
	global_store_dwordx4 v[28:29], v[24:27], off
	s_waitcnt lgkmcnt(0)
	s_branch .LBB0_72

; __device__ __forceinline__ void ada_unit(KP Pk, Frame& F, int u) {
;     ...
; #pragma unroll 1
;     for (int k0 = 0; k0 < 64; k0 += 16) {
;         f32x4 w[16];
; #pragma unroll
;         for (int q = 0; q < 16; ++q) w[q] = W[(size_t)(k0 + q) * 3072];
; #pragma unroll
;         for (int q = 0; q < 16; ++q) {
; #pragma unroll
;             for (int r = 0; r < 9; ++r) a[r] += w[q] * sc[r * 128 + kh * 64 + k0 + q];
;             if ((q & 3) == 3) __builtin_amdgcn_sched_barrier(0); }
.LBB0_95:
	v_add_co_u32_e32 v0, vcc, s60, v78
	v_mov_b32_e32 v146, s28
	s_nop 0
	v_addc_co_u32_e32 v1, vcc, -1, v79, vcc
	global_load_dwordx4 v[86:89], v[0:1], off nt
	v_add_co_u32_e32 v0, vcc, s61, v78
	s_nop 1
	v_addc_co_u32_e32 v1, vcc, -1, v79, vcc
	v_add_co_u32_e32 v2, vcc, s62, v78
	global_load_dwordx4 v[90:93], v[0:1], off nt
	s_nop 0
	v_addc_co_u32_e32 v3, vcc, -1, v79, vcc
	v_add_co_u32_e32 v4, vcc, s63, v78
	global_load_dwordx4 v[94:97], v[2:3], off nt
	s_nop 0
	v_addc_co_u32_e32 v5, vcc, -1, v79, vcc
	v_add_co_u32_e32 v6, vcc, s64, v78
	global_load_dwordx4 v[98:101], v[4:5], off nt
	global_load_dwordx4 v[0:3], v[78:79], off nt
	v_addc_co_u32_e32 v7, vcc, -1, v79, vcc
	v_add_co_u32_e32 v8, vcc, s65, v78
	s_nop 1
	v_addc_co_u32_e32 v9, vcc, -1, v79, vcc
	v_add_co_u32_e32 v10, vcc, s66, v78
	s_nop 1
	v_addc_co_u32_e32 v11, vcc, -1, v79, vcc
	v_add_co_u32_e32 v20, vcc, s67, v78
	s_nop 1
	v_addc_co_u32_e32 v21, vcc, -1, v79, vcc
	v_add_co_u32_e32 v22, vcc, s52, v78
	s_nop 1
	v_addc_co_u32_e32 v23, vcc, -1, v79, vcc
	v_add_co_u32_e32 v36, vcc, s68, v78
	s_nop 1
	v_addc_co_u32_e32 v37, vcc, -1, v79, vcc
	v_add_co_u32_e32 v38, vcc, s70, v78
	s_nop 1
	v_addc_co_u32_e32 v39, vcc, -1, v79, vcc
	v_add_co_u32_e32 v110, vcc, s71, v78
	s_nop 1
	v_addc_co_u32_e32 v111, vcc, -1, v79, vcc
	global_load_dwordx4 v[102:105], v[6:7], off nt
	global_load_dwordx4 v[106:109], v[8:9], off nt
	global_load_dwordx4 v[72:75], v[10:11], off nt
	global_load_dwordx4 v[68:71], v[20:21], off nt
	global_load_dwordx4 v[64:67], v[22:23], off nt
	global_load_dwordx4 v[60:63], v[36:37], off nt
	global_load_dwordx4 v[48:51], v[38:39], off nt
	s_nop 0
	global_load_dwordx4 v[36:39], v[110:111], off nt
	v_add_co_u32_e32 v114, vcc, s72, v78
	ds_read_b128 v[110:113], v146
	s_nop 0
	v_addc_co_u32_e32 v115, vcc, -1, v79, vcc
	v_add_co_u32_e32 v116, vcc, s73, v78
	s_waitcnt vmcnt(12) lgkmcnt(0)
	v_pk_fma_f32 v[130:131], v[86:87], v[110:111], v[56:57] op_sel_hi:[1,0,1]
	v_addc_co_u32_e32 v117, vcc, -1, v79, vcc
	v_add_co_u32_e32 v4, vcc, s74, v78
	global_load_dwordx4 v[20:23], v[114:115], off nt
	global_load_dwordx4 v[8:11], v[116:117], off nt
	v_addc_co_u32_e32 v5, vcc, -1, v79, vcc
	global_load_dwordx4 v[4:7], v[4:5], off nt
	ds_read_b128 v[114:117], v146 offset:512
	ds_read_b128 v[118:121], v146 offset:1024
	ds_read_b128 v[122:125], v146 offset:2048
	ds_read_b128 v[126:129], v146 offset:3584
	v_pk_fma_f32 v[58:59], v[88:89], v[110:111], v[58:59] op_sel_hi:[1,0,1]
	s_waitcnt lgkmcnt(3)
	v_pk_fma_f32 v[132:133], v[88:89], v[114:115], v[54:55] op_sel_hi:[1,0,1]
	ds_read_b128 v[54:57], v146 offset:1536
	s_waitcnt lgkmcnt(3)
	v_pk_fma_f32 v[134:135], v[86:87], v[118:119], v[44:45] op_sel_hi:[1,0,1]
	s_waitcnt lgkmcnt(2)
	v_pk_fma_f32 v[138:139], v[88:89], v[122:123], v[34:35] op_sel_hi:[1,0,1]
	v_pk_fma_f32 v[140:141], v[86:87], v[122:123], v[32:33] op_sel_hi:[1,0,1]
	ds_read_b128 v[32:35], v146 offset:3072
	s_waitcnt lgkmcnt(1)
	v_pk_fma_f32 v[136:137], v[88:89], v[54:55], v[42:43] op_sel_hi:[1,0,1]
	ds_read_b128 v[42:45], v146 offset:2560
	v_pk_fma_f32 v[52:53], v[86:87], v[114:115], v[52:53] op_sel_hi:[1,0,1]
	v_pk_fma_f32 v[40:41], v[86:87], v[54:55], v[40:41] op_sel_hi:[1,0,1]
	s_waitcnt lgkmcnt(1)
	v_pk_fma_f32 v[26:27], v[88:89], v[32:33], v[26:27] op_sel_hi:[1,0,1]
	v_pk_fma_f32 v[24:25], v[86:87], v[32:33], v[24:25] op_sel_hi:[1,0,1]
	s_waitcnt lgkmcnt(0)
	v_pk_fma_f32 v[142:143], v[88:89], v[42:43], v[30:31] op_sel_hi:[1,0,1]
	v_pk_fma_f32 v[144:145], v[86:87], v[42:43], v[28:29] op_sel_hi:[1,0,1]
	ds_read_b128 v[28:31], v146 offset:4096
	v_pk_fma_f32 v[16:17], v[86:87], v[126:127], v[16:17] op_sel_hi:[1,0,1]
	s_waitcnt vmcnt(14)
	v_pk_fma_f32 v[58:59], v[92:93], v[110:111], v[58:59] op_sel:[0,1,0]
	v_pk_fma_f32 v[46:47], v[88:89], v[118:119], v[46:47] op_sel_hi:[1,0,1]
	v_pk_fma_f32 v[18:19], v[88:89], v[126:127], v[18:19] op_sel_hi:[1,0,1]
	s_waitcnt lgkmcnt(0)
	v_pk_fma_f32 v[14:15], v[88:89], v[28:29], v[14:15] op_sel_hi:[1,0,1]
	v_pk_fma_f32 v[12:13], v[86:87], v[28:29], v[12:13] op_sel_hi:[1,0,1]
	v_pk_fma_f32 v[86:87], v[90:91], v[110:111], v[130:131] op_sel:[0,1,0]
	v_pk_fma_f32 v[14:15], v[92:93], v[28:29], v[14:15] op_sel:[0,1,0]
	v_pk_fma_f32 v[12:13], v[90:91], v[28:29], v[12:13] op_sel:[0,1,0]
	v_pk_fma_f32 v[88:89], v[92:93], v[114:115], v[132:133] op_sel:[0,1,0]
	v_pk_fma_f32 v[52:53], v[90:91], v[114:115], v[52:53] op_sel:[0,1,0]
	v_pk_fma_f32 v[26:27], v[92:93], v[32:33], v[26:27] op_sel:[0,1,0]
	v_pk_fma_f32 v[24:25], v[90:91], v[32:33], v[24:25] op_sel:[0,1,0]
	s_waitcnt vmcnt(13)
	v_pk_fma_f32 v[28:29], v[96:97], v[112:113], v[58:59] op_sel_hi:[1,0,1]
	v_pk_fma_f32 v[32:33], v[94:95], v[112:113], v[86:87] op_sel_hi:[1,0,1]
	v_pk_fma_f32 v[14:15], v[96:97], v[30:31], v[14:15] op_sel_hi:[1,0,1]
	v_pk_fma_f32 v[12:13], v[94:95], v[30:31], v[12:13] op_sel_hi:[1,0,1]
	v_mov_b32_e32 v30, v113
	v_pk_fma_f32 v[46:47], v[92:93], v[118:119], v[46:47] op_sel:[0,1,0]
	v_pk_fma_f32 v[110:111], v[90:91], v[118:119], v[134:135] op_sel:[0,1,0]
	v_pk_fma_f32 v[58:59], v[96:97], v[116:117], v[88:89] op_sel_hi:[1,0,1]
	v_pk_fma_f32 v[52:53], v[94:95], v[116:117], v[52:53] op_sel_hi:[1,0,1]
	s_waitcnt vmcnt(12)
; __device__ __forceinline__ void ada_unit(KP Pk, Frame& F, int u) {
;     ...
; #pragma unroll
;         for (int q = 0; q < 16; ++q) {
; #pragma unroll
;             for (int r = 0; r < 9; ++r) a[r] += w[q] * sc[r * 128 + kh * 64 + k0 + q];
;             if ((q & 3) == 3) __builtin_amdgcn_sched_barrier(0); }
	v_pk_fma_f32 v[28:29], v[100:101], v[30:31], v[28:29] op_sel_hi:[1,0,1]
	v_pk_fma_f32 v[32:33], v[98:99], v[30:31], v[32:33] op_sel_hi:[1,0,1]
	v_mov_b32_e32 v30, v117
	v_pk_fma_f32 v[114:115], v[92:93], v[54:55], v[136:137] op_sel:[0,1,0]
	v_pk_fma_f32 v[40:41], v[90:91], v[54:55], v[40:41] op_sel:[0,1,0]
	v_pk_fma_f32 v[46:47], v[96:97], v[120:121], v[46:47] op_sel_hi:[1,0,1]
	v_pk_fma_f32 v[86:87], v[94:95], v[120:121], v[110:111] op_sel_hi:[1,0,1]
	v_pk_fma_f32 v[58:59], v[100:101], v[30:31], v[58:59] op_sel_hi:[1,0,1]
	v_pk_fma_f32 v[52:53], v[98:99], v[30:31], v[52:53] op_sel_hi:[1,0,1]
	v_mov_b32_e32 v30, v121
	v_pk_fma_f32 v[54:55], v[92:93], v[122:123], v[138:139] op_sel:[0,1,0]
	v_pk_fma_f32 v[118:119], v[90:91], v[122:123], v[140:141] op_sel:[0,1,0]
	v_pk_fma_f32 v[88:89], v[96:97], v[56:57], v[114:115] op_sel_hi:[1,0,1]
	v_pk_fma_f32 v[40:41], v[94:95], v[56:57], v[40:41] op_sel_hi:[1,0,1]
	v_pk_fma_f32 v[46:47], v[100:101], v[30:31], v[46:47] op_sel_hi:[1,0,1]
	v_pk_fma_f32 v[86:87], v[98:99], v[30:31], v[86:87] op_sel_hi:[1,0,1]
	v_mov_b32_e32 v30, v57
	v_pk_fma_f32 v[122:123], v[92:93], v[42:43], v[142:143] op_sel:[0,1,0]
	v_pk_fma_f32 v[42:43], v[90:91], v[42:43], v[144:145] op_sel:[0,1,0]
	v_pk_fma_f32 v[16:17], v[90:91], v[126:127], v[16:17] op_sel:[0,1,0]
	v_pk_fma_f32 v[54:55], v[96:97], v[124:125], v[54:55] op_sel_hi:[1,0,1]
	v_pk_fma_f32 v[90:91], v[94:95], v[124:125], v[118:119] op_sel_hi:[1,0,1]
	v_pk_fma_f32 v[56:57], v[100:101], v[30:31], v[88:89] op_sel_hi:[1,0,1]
	v_pk_fma_f32 v[88:89], v[98:99], v[30:31], v[40:41] op_sel_hi:[1,0,1]
	v_mov_b32_e32 v30, v125
	v_pk_fma_f32 v[18:19], v[92:93], v[126:127], v[18:19] op_sel:[0,1,0]
	v_pk_fma_f32 v[92:93], v[96:97], v[44:45], v[122:123] op_sel_hi:[1,0,1]
	v_pk_fma_f32 v[42:43], v[94:95], v[44:45], v[42:43] op_sel_hi:[1,0,1]
	v_pk_fma_f32 v[54:55], v[100:101], v[30:31], v[54:55] op_sel_hi:[1,0,1]
	v_pk_fma_f32 v[90:91], v[98:99], v[30:31], v[90:91] op_sel_hi:[1,0,1]
	v_mov_b32_e32 v30, v45
	v_pk_fma_f32 v[24:25], v[94:95], v[34:35], v[24:25] op_sel_hi:[1,0,1]
	v_pk_fma_f32 v[16:17], v[94:95], v[128:129], v[16:17] op_sel_hi:[1,0,1]
	v_pk_fma_f32 v[92:93], v[100:101], v[30:31], v[92:93] op_sel_hi:[1,0,1]
	v_pk_fma_f32 v[94:95], v[98:99], v[30:31], v[42:43] op_sel_hi:[1,0,1]
	v_mov_b32_e32 v30, v35
	v_pk_fma_f32 v[110:111], v[98:99], v[30:31], v[24:25] op_sel_hi:[1,0,1]
	v_mov_b32_e32 v24, v129
	v_pk_fma_f32 v[26:27], v[96:97], v[34:35], v[26:27] op_sel_hi:[1,0,1]
	v_pk_fma_f32 v[18:19], v[96:97], v[128:129], v[18:19] op_sel_hi:[1,0,1]
	v_pk_fma_f32 v[114:115], v[98:99], v[24:25], v[16:17] op_sel_hi:[1,0,1]
	v_mov_b32_e32 v16, v31
	v_pk_fma_f32 v[96:97], v[100:101], v[30:31], v[26:27] op_sel_hi:[1,0,1]
	v_pk_fma_f32 v[112:113], v[100:101], v[24:25], v[18:19] op_sel_hi:[1,0,1]
	v_pk_fma_f32 v[100:101], v[100:101], v[16:17], v[14:15] op_sel_hi:[1,0,1]
	v_pk_fma_f32 v[98:99], v[98:99], v[16:17], v[12:13] op_sel_hi:[1,0,1]
	ds_read_b128 v[12:15], v146 offset:16
	ds_read_b128 v[16:19], v146 offset:528
	ds_read_b128 v[24:27], v146 offset:1040
	ds_read_b128 v[40:43], v146 offset:2576
	s_waitcnt vmcnt(10) lgkmcnt(3)
	v_pk_fma_f32 v[116:117], v[104:105], v[12:13], v[28:29] op_sel_hi:[1,0,1]
	v_pk_fma_f32 v[118:119], v[102:103], v[12:13], v[32:33] op_sel_hi:[1,0,1]
	ds_read_b128 v[28:31], v146 offset:1552
	ds_read_b128 v[32:35], v146 offset:2064
	s_waitcnt lgkmcnt(4)
	v_pk_fma_f32 v[120:121], v[104:105], v[16:17], v[58:59] op_sel_hi:[1,0,1]
	v_pk_fma_f32 v[122:123], v[102:103], v[16:17], v[52:53] op_sel_hi:[1,0,1]
	s_waitcnt lgkmcnt(3)
	v_pk_fma_f32 v[124:125], v[104:105], v[24:25], v[46:47] op_sel_hi:[1,0,1]
	s_waitcnt lgkmcnt(1)
	v_pk_fma_f32 v[126:127], v[104:105], v[28:29], v[56:57] op_sel_hi:[1,0,1]
	s_waitcnt lgkmcnt(0)
	v_pk_fma_f32 v[128:129], v[104:105], v[32:33], v[54:55] op_sel_hi:[1,0,1]
	ds_read_b128 v[44:47], v146 offset:3088
	ds_read_b128 v[52:55], v146 offset:3600
	ds_read_b128 v[56:59], v146 offset:4112
	v_pk_fma_f32 v[86:87], v[102:103], v[24:25], v[86:87] op_sel_hi:[1,0,1]
	v_pk_fma_f32 v[88:89], v[102:103], v[28:29], v[88:89] op_sel_hi:[1,0,1]
	v_pk_fma_f32 v[90:91], v[102:103], v[32:33], v[90:91] op_sel_hi:[1,0,1]
	v_pk_fma_f32 v[92:93], v[104:105], v[40:41], v[92:93] op_sel_hi:[1,0,1]
	v_pk_fma_f32 v[94:95], v[102:103], v[40:41], v[94:95] op_sel_hi:[1,0,1]
	s_waitcnt lgkmcnt(2)
	v_pk_fma_f32 v[96:97], v[104:105], v[44:45], v[96:97] op_sel_hi:[1,0,1]
	v_pk_fma_f32 v[110:111], v[102:103], v[44:45], v[110:111] op_sel_hi:[1,0,1]
	s_waitcnt lgkmcnt(1)
	v_pk_fma_f32 v[112:113], v[104:105], v[52:53], v[112:113] op_sel_hi:[1,0,1]
	v_pk_fma_f32 v[114:115], v[102:103], v[52:53], v[114:115] op_sel_hi:[1,0,1]
	s_waitcnt lgkmcnt(0)
	v_pk_fma_f32 v[100:101], v[104:105], v[56:57], v[100:101] op_sel_hi:[1,0,1]
	v_pk_fma_f32 v[98:99], v[102:103], v[56:57], v[98:99] op_sel_hi:[1,0,1]
	s_waitcnt vmcnt(9)
	v_pk_fma_f32 v[102:103], v[108:109], v[12:13], v[116:117] op_sel:[0,1,0]
	v_pk_fma_f32 v[12:13], v[106:107], v[12:13], v[118:119] op_sel:[0,1,0]
	v_pk_fma_f32 v[104:105], v[108:109], v[16:17], v[120:121] op_sel:[0,1,0]
	v_pk_fma_f32 v[16:17], v[106:107], v[16:17], v[122:123] op_sel:[0,1,0]
	v_pk_fma_f32 v[116:117], v[108:109], v[24:25], v[124:125] op_sel:[0,1,0]
	v_pk_fma_f32 v[24:25], v[106:107], v[24:25], v[86:87] op_sel:[0,1,0]
	v_pk_fma_f32 v[86:87], v[108:109], v[28:29], v[126:127] op_sel:[0,1,0]
	v_pk_fma_f32 v[28:29], v[106:107], v[28:29], v[88:89] op_sel:[0,1,0]
	v_pk_fma_f32 v[88:89], v[108:109], v[32:33], v[128:129] op_sel:[0,1,0]
	v_pk_fma_f32 v[32:33], v[106:107], v[32:33], v[90:91] op_sel:[0,1,0]
	v_pk_fma_f32 v[90:91], v[108:109], v[40:41], v[92:93] op_sel:[0,1,0]
	v_pk_fma_f32 v[40:41], v[106:107], v[40:41], v[94:95] op_sel:[0,1,0]
	v_pk_fma_f32 v[92:93], v[108:109], v[44:45], v[96:97] op_sel:[0,1,0]
	v_pk_fma_f32 v[94:95], v[108:109], v[52:53], v[112:113] op_sel:[0,1,0]
	v_pk_fma_f32 v[96:97], v[108:109], v[56:57], v[100:101] op_sel:[0,1,0]
	v_pk_fma_f32 v[56:57], v[106:107], v[56:57], v[98:99] op_sel:[0,1,0]
	s_waitcnt vmcnt(8)
; __device__ __forceinline__ void ada_unit(KP Pk, Frame& F, int u) {
;     ...
; #pragma unroll
;         for (int q = 0; q < 16; ++q) {
; #pragma unroll
;             for (int r = 0; r < 9; ++r) a[r] += w[q] * sc[r * 128 + kh * 64 + k0 + q];
;             if ((q & 3) == 3) __builtin_amdgcn_sched_barrier(0); }
	v_pk_fma_f32 v[98:99], v[74:75], v[14:15], v[102:103] op_sel_hi:[1,0,1]
	v_pk_fma_f32 v[12:13], v[72:73], v[14:15], v[12:13] op_sel_hi:[1,0,1]
	v_mov_b32_e32 v14, v15
	v_pk_fma_f32 v[44:45], v[106:107], v[44:45], v[110:111] op_sel:[0,1,0]
	v_pk_fma_f32 v[52:53], v[106:107], v[52:53], v[114:115] op_sel:[0,1,0]
	v_pk_fma_f32 v[100:101], v[74:75], v[18:19], v[104:105] op_sel_hi:[1,0,1]
	v_pk_fma_f32 v[16:17], v[72:73], v[18:19], v[16:17] op_sel_hi:[1,0,1]
	v_pk_fma_f32 v[102:103], v[74:75], v[26:27], v[116:117] op_sel_hi:[1,0,1]
	v_pk_fma_f32 v[86:87], v[74:75], v[30:31], v[86:87] op_sel_hi:[1,0,1]
	v_pk_fma_f32 v[88:89], v[74:75], v[34:35], v[88:89] op_sel_hi:[1,0,1]
	v_pk_fma_f32 v[90:91], v[74:75], v[42:43], v[90:91] op_sel_hi:[1,0,1]
	v_pk_fma_f32 v[92:93], v[74:75], v[46:47], v[92:93] op_sel_hi:[1,0,1]
	v_pk_fma_f32 v[94:95], v[74:75], v[54:55], v[94:95] op_sel_hi:[1,0,1]
	v_pk_fma_f32 v[74:75], v[74:75], v[58:59], v[96:97] op_sel_hi:[1,0,1]
	s_waitcnt vmcnt(7)
	v_pk_fma_f32 v[96:97], v[68:69], v[14:15], v[12:13] op_sel_hi:[1,0,1]
	v_mov_b32_e32 v12, v19
	v_pk_fma_f32 v[24:25], v[72:73], v[26:27], v[24:25] op_sel_hi:[1,0,1]
	v_pk_fma_f32 v[28:29], v[72:73], v[30:31], v[28:29] op_sel_hi:[1,0,1]
	v_pk_fma_f32 v[32:33], v[72:73], v[34:35], v[32:33] op_sel_hi:[1,0,1]
	v_pk_fma_f32 v[40:41], v[72:73], v[42:43], v[40:41] op_sel_hi:[1,0,1]
	v_pk_fma_f32 v[44:45], v[72:73], v[46:47], v[44:45] op_sel_hi:[1,0,1]
	v_pk_fma_f32 v[52:53], v[72:73], v[54:55], v[52:53] op_sel_hi:[1,0,1]
	v_pk_fma_f32 v[56:57], v[72:73], v[58:59], v[56:57] op_sel_hi:[1,0,1]
	v_pk_fma_f32 v[72:73], v[70:71], v[14:15], v[98:99] op_sel_hi:[1,0,1]
	v_pk_fma_f32 v[98:99], v[70:71], v[12:13], v[100:101] op_sel_hi:[1,0,1]
	v_pk_fma_f32 v[100:101], v[68:69], v[12:13], v[16:17] op_sel_hi:[1,0,1]
	v_mov_b32_e32 v12, v27
	v_pk_fma_f32 v[102:103], v[70:71], v[12:13], v[102:103] op_sel_hi:[1,0,1]
	v_pk_fma_f32 v[104:105], v[68:69], v[12:13], v[24:25] op_sel_hi:[1,0,1]
	v_mov_b32_e32 v12, v31
	v_pk_fma_f32 v[86:87], v[70:71], v[12:13], v[86:87] op_sel_hi:[1,0,1]
	v_pk_fma_f32 v[106:107], v[68:69], v[12:13], v[28:29] op_sel_hi:[1,0,1]
	v_mov_b32_e32 v12, v35
	v_pk_fma_f32 v[88:89], v[70:71], v[12:13], v[88:89] op_sel_hi:[1,0,1]
	v_pk_fma_f32 v[108:109], v[68:69], v[12:13], v[32:33] op_sel_hi:[1,0,1]
	v_mov_b32_e32 v12, v43
	v_pk_fma_f32 v[90:91], v[70:71], v[12:13], v[90:91] op_sel_hi:[1,0,1]
	v_pk_fma_f32 v[110:111], v[68:69], v[12:13], v[40:41] op_sel_hi:[1,0,1]
	v_mov_b32_e32 v12, v47
	v_pk_fma_f32 v[92:93], v[70:71], v[12:13], v[92:93] op_sel_hi:[1,0,1]
	v_pk_fma_f32 v[112:113], v[68:69], v[12:13], v[44:45] op_sel_hi:[1,0,1]
	v_mov_b32_e32 v12, v55
	v_pk_fma_f32 v[94:95], v[70:71], v[12:13], v[94:95] op_sel_hi:[1,0,1]
	v_pk_fma_f32 v[114:115], v[68:69], v[12:13], v[52:53] op_sel_hi:[1,0,1]
	v_mov_b32_e32 v12, v59
	v_pk_fma_f32 v[70:71], v[70:71], v[12:13], v[74:75] op_sel_hi:[1,0,1]
	v_pk_fma_f32 v[68:69], v[68:69], v[12:13], v[56:57] op_sel_hi:[1,0,1]
	ds_read_b128 v[12:15], v146 offset:32
	ds_read_b128 v[16:19], v146 offset:544
	ds_read_b128 v[24:27], v146 offset:1056
	ds_read_b128 v[28:31], v146 offset:1568
	ds_read_b128 v[32:35], v146 offset:2080
	ds_read_b128 v[40:43], v146 offset:2592
	ds_read_b128 v[44:47], v146 offset:3104
	ds_read_b128 v[52:55], v146 offset:3616
	ds_read_b128 v[56:59], v146 offset:4128
	s_waitcnt vmcnt(6) lgkmcnt(8)
	v_pk_fma_f32 v[72:73], v[66:67], v[12:13], v[72:73] op_sel_hi:[1,0,1]
	v_pk_fma_f32 v[74:75], v[64:65], v[12:13], v[96:97] op_sel_hi:[1,0,1]
	s_waitcnt lgkmcnt(7)
	v_pk_fma_f32 v[96:97], v[66:67], v[16:17], v[98:99] op_sel_hi:[1,0,1]
	v_pk_fma_f32 v[98:99], v[64:65], v[16:17], v[100:101] op_sel_hi:[1,0,1]
	s_waitcnt lgkmcnt(6)
	v_pk_fma_f32 v[100:101], v[66:67], v[24:25], v[102:103] op_sel_hi:[1,0,1]
	v_pk_fma_f32 v[102:103], v[64:65], v[24:25], v[104:105] op_sel_hi:[1,0,1]
	s_waitcnt lgkmcnt(5)
	v_pk_fma_f32 v[86:87], v[66:67], v[28:29], v[86:87] op_sel_hi:[1,0,1]
	v_pk_fma_f32 v[104:105], v[64:65], v[28:29], v[106:107] op_sel_hi:[1,0,1]
	s_waitcnt lgkmcnt(4)
	v_pk_fma_f32 v[88:89], v[66:67], v[32:33], v[88:89] op_sel_hi:[1,0,1]
	v_pk_fma_f32 v[106:107], v[64:65], v[32:33], v[108:109] op_sel_hi:[1,0,1]
	s_waitcnt lgkmcnt(3)
	v_pk_fma_f32 v[90:91], v[66:67], v[40:41], v[90:91] op_sel_hi:[1,0,1]
	v_pk_fma_f32 v[108:109], v[64:65], v[40:41], v[110:111] op_sel_hi:[1,0,1]
	s_waitcnt lgkmcnt(2)
	v_pk_fma_f32 v[92:93], v[66:67], v[44:45], v[92:93] op_sel_hi:[1,0,1]
	v_pk_fma_f32 v[110:111], v[64:65], v[44:45], v[112:113] op_sel_hi:[1,0,1]
	s_waitcnt lgkmcnt(1)
	v_pk_fma_f32 v[94:95], v[66:67], v[52:53], v[94:95] op_sel_hi:[1,0,1]
	v_pk_fma_f32 v[112:113], v[64:65], v[52:53], v[114:115] op_sel_hi:[1,0,1]
	s_waitcnt lgkmcnt(0)
	v_pk_fma_f32 v[66:67], v[66:67], v[56:57], v[70:71] op_sel_hi:[1,0,1]
	v_pk_fma_f32 v[64:65], v[64:65], v[56:57], v[68:69] op_sel_hi:[1,0,1]
	s_waitcnt vmcnt(5)
	v_pk_fma_f32 v[68:69], v[62:63], v[12:13], v[72:73] op_sel:[0,1,0]
	v_pk_fma_f32 v[12:13], v[60:61], v[12:13], v[74:75] op_sel:[0,1,0]
	v_pk_fma_f32 v[70:71], v[62:63], v[16:17], v[96:97] op_sel:[0,1,0]
	v_pk_fma_f32 v[16:17], v[60:61], v[16:17], v[98:99] op_sel:[0,1,0]
	v_pk_fma_f32 v[72:73], v[62:63], v[24:25], v[100:101] op_sel:[0,1,0]
	v_pk_fma_f32 v[24:25], v[60:61], v[24:25], v[102:103] op_sel:[0,1,0]
	v_pk_fma_f32 v[74:75], v[62:63], v[28:29], v[86:87] op_sel:[0,1,0]
	v_pk_fma_f32 v[28:29], v[60:61], v[28:29], v[104:105] op_sel:[0,1,0]
	v_pk_fma_f32 v[86:87], v[62:63], v[32:33], v[88:89] op_sel:[0,1,0]
	v_pk_fma_f32 v[32:33], v[60:61], v[32:33], v[106:107] op_sel:[0,1,0]
	v_pk_fma_f32 v[88:89], v[62:63], v[40:41], v[90:91] op_sel:[0,1,0]
	v_pk_fma_f32 v[40:41], v[60:61], v[40:41], v[108:109] op_sel:[0,1,0]
	v_pk_fma_f32 v[90:91], v[62:63], v[44:45], v[92:93] op_sel:[0,1,0]
	v_pk_fma_f32 v[44:45], v[60:61], v[44:45], v[110:111] op_sel:[0,1,0]
	v_pk_fma_f32 v[92:93], v[62:63], v[52:53], v[94:95] op_sel:[0,1,0]
	v_pk_fma_f32 v[52:53], v[60:61], v[52:53], v[112:113] op_sel:[0,1,0]
	v_pk_fma_f32 v[62:63], v[62:63], v[56:57], v[66:67] op_sel:[0,1,0]
	v_pk_fma_f32 v[56:57], v[60:61], v[56:57], v[64:65] op_sel:[0,1,0]
	s_waitcnt vmcnt(4)
; __device__ __forceinline__ void ada_unit(KP Pk, Frame& F, int u) {
;     ...
; #pragma unroll
;         for (int q = 0; q < 16; ++q) {
; #pragma unroll
;             for (int r = 0; r < 9; ++r) a[r] += w[q] * sc[r * 128 + kh * 64 + k0 + q];
;             if ((q & 3) == 3) __builtin_amdgcn_sched_barrier(0); }
	v_pk_fma_f32 v[60:61], v[50:51], v[14:15], v[68:69] op_sel_hi:[1,0,1]
	v_pk_fma_f32 v[12:13], v[48:49], v[14:15], v[12:13] op_sel_hi:[1,0,1]
	v_mov_b32_e32 v14, v15
	v_pk_fma_f32 v[64:65], v[50:51], v[18:19], v[70:71] op_sel_hi:[1,0,1]
	v_pk_fma_f32 v[16:17], v[48:49], v[18:19], v[16:17] op_sel_hi:[1,0,1]
	v_pk_fma_f32 v[24:25], v[48:49], v[26:27], v[24:25] op_sel_hi:[1,0,1]
	v_pk_fma_f32 v[28:29], v[48:49], v[30:31], v[28:29] op_sel_hi:[1,0,1]
	v_pk_fma_f32 v[32:33], v[48:49], v[34:35], v[32:33] op_sel_hi:[1,0,1]
	v_pk_fma_f32 v[40:41], v[48:49], v[42:43], v[40:41] op_sel_hi:[1,0,1]
	v_pk_fma_f32 v[44:45], v[48:49], v[46:47], v[44:45] op_sel_hi:[1,0,1]
	v_pk_fma_f32 v[52:53], v[48:49], v[54:55], v[52:53] op_sel_hi:[1,0,1]
	v_pk_fma_f32 v[48:49], v[48:49], v[58:59], v[56:57] op_sel_hi:[1,0,1]
	s_waitcnt vmcnt(3)
	v_pk_fma_f32 v[56:57], v[38:39], v[14:15], v[60:61] op_sel_hi:[1,0,1]
	v_pk_fma_f32 v[60:61], v[36:37], v[14:15], v[12:13] op_sel_hi:[1,0,1]
	v_mov_b32_e32 v12, v19
	v_pk_fma_f32 v[66:67], v[50:51], v[26:27], v[72:73] op_sel_hi:[1,0,1]
	v_pk_fma_f32 v[68:69], v[50:51], v[30:31], v[74:75] op_sel_hi:[1,0,1]
	v_pk_fma_f32 v[70:71], v[50:51], v[34:35], v[86:87] op_sel_hi:[1,0,1]
	v_pk_fma_f32 v[72:73], v[50:51], v[42:43], v[88:89] op_sel_hi:[1,0,1]
	v_pk_fma_f32 v[74:75], v[50:51], v[46:47], v[90:91] op_sel_hi:[1,0,1]
	v_pk_fma_f32 v[86:87], v[50:51], v[54:55], v[92:93] op_sel_hi:[1,0,1]
	v_pk_fma_f32 v[50:51], v[50:51], v[58:59], v[62:63] op_sel_hi:[1,0,1]
	v_pk_fma_f32 v[62:63], v[38:39], v[12:13], v[64:65] op_sel_hi:[1,0,1]
	v_pk_fma_f32 v[64:65], v[36:37], v[12:13], v[16:17] op_sel_hi:[1,0,1]
	v_mov_b32_e32 v12, v27
	v_pk_fma_f32 v[66:67], v[38:39], v[12:13], v[66:67] op_sel_hi:[1,0,1]
	v_pk_fma_f32 v[88:89], v[36:37], v[12:13], v[24:25] op_sel_hi:[1,0,1]
	v_mov_b32_e32 v12, v31
	v_pk_fma_f32 v[68:69], v[38:39], v[12:13], v[68:69] op_sel_hi:[1,0,1]
	v_pk_fma_f32 v[90:91], v[36:37], v[12:13], v[28:29] op_sel_hi:[1,0,1]
	v_mov_b32_e32 v12, v35
	v_pk_fma_f32 v[70:71], v[38:39], v[12:13], v[70:71] op_sel_hi:[1,0,1]
	v_pk_fma_f32 v[92:93], v[36:37], v[12:13], v[32:33] op_sel_hi:[1,0,1]
	v_mov_b32_e32 v12, v43
	v_pk_fma_f32 v[42:43], v[38:39], v[12:13], v[72:73] op_sel_hi:[1,0,1]
	v_pk_fma_f32 v[40:41], v[36:37], v[12:13], v[40:41] op_sel_hi:[1,0,1]
	v_mov_b32_e32 v12, v47
	v_pk_fma_f32 v[72:73], v[38:39], v[12:13], v[74:75] op_sel_hi:[1,0,1]
	v_pk_fma_f32 v[44:45], v[36:37], v[12:13], v[44:45] op_sel_hi:[1,0,1]
	v_mov_b32_e32 v12, v55
	v_pk_fma_f32 v[54:55], v[38:39], v[12:13], v[86:87] op_sel_hi:[1,0,1]
	v_pk_fma_f32 v[52:53], v[36:37], v[12:13], v[52:53] op_sel_hi:[1,0,1]
	v_mov_b32_e32 v12, v59
	v_pk_fma_f32 v[50:51], v[38:39], v[12:13], v[50:51] op_sel_hi:[1,0,1]
	v_pk_fma_f32 v[74:75], v[36:37], v[12:13], v[48:49] op_sel_hi:[1,0,1]
	ds_read_b128 v[12:15], v146 offset:48
	ds_read_b128 v[16:19], v146 offset:560
	ds_read_b128 v[24:27], v146 offset:1072
	ds_read_b128 v[28:31], v146 offset:1584
	ds_read_b128 v[32:35], v146 offset:2096
	s_waitcnt vmcnt(2) lgkmcnt(4)
	v_pk_fma_f32 v[86:87], v[20:21], v[12:13], v[60:61] op_sel_hi:[1,0,1]
	s_waitcnt lgkmcnt(3)
	v_pk_fma_f32 v[94:95], v[22:23], v[16:17], v[62:63] op_sel_hi:[1,0,1]
	v_pk_fma_f32 v[96:97], v[20:21], v[16:17], v[64:65] op_sel_hi:[1,0,1]
	ds_read_b128 v[36:39], v146 offset:2608
	ds_read_b128 v[46:49], v146 offset:3120
	ds_read_b128 v[58:61], v146 offset:3632
	ds_read_b128 v[62:65], v146 offset:4144
	v_pk_fma_f32 v[56:57], v[22:23], v[12:13], v[56:57] op_sel_hi:[1,0,1]
	s_waitcnt lgkmcnt(6)
	v_pk_fma_f32 v[66:67], v[22:23], v[24:25], v[66:67] op_sel_hi:[1,0,1]
	v_pk_fma_f32 v[88:89], v[20:21], v[24:25], v[88:89] op_sel_hi:[1,0,1]
	s_waitcnt lgkmcnt(5)
	v_pk_fma_f32 v[68:69], v[22:23], v[28:29], v[68:69] op_sel_hi:[1,0,1]
	v_pk_fma_f32 v[90:91], v[20:21], v[28:29], v[90:91] op_sel_hi:[1,0,1]
	s_waitcnt lgkmcnt(4)
	v_pk_fma_f32 v[70:71], v[22:23], v[32:33], v[70:71] op_sel_hi:[1,0,1]
	v_pk_fma_f32 v[92:93], v[20:21], v[32:33], v[92:93] op_sel_hi:[1,0,1]
	s_waitcnt lgkmcnt(3)
	v_pk_fma_f32 v[42:43], v[22:23], v[36:37], v[42:43] op_sel_hi:[1,0,1]
	v_pk_fma_f32 v[40:41], v[20:21], v[36:37], v[40:41] op_sel_hi:[1,0,1]
	s_waitcnt lgkmcnt(2)
	v_pk_fma_f32 v[44:45], v[20:21], v[46:47], v[44:45] op_sel_hi:[1,0,1]
	s_waitcnt lgkmcnt(1)
	v_pk_fma_f32 v[52:53], v[20:21], v[58:59], v[52:53] op_sel_hi:[1,0,1]
	s_waitcnt lgkmcnt(0)
	v_pk_fma_f32 v[20:21], v[20:21], v[62:63], v[74:75] op_sel_hi:[1,0,1]
	v_pk_fma_f32 v[72:73], v[22:23], v[46:47], v[72:73] op_sel_hi:[1,0,1]
	v_pk_fma_f32 v[54:55], v[22:23], v[58:59], v[54:55] op_sel_hi:[1,0,1]
	v_pk_fma_f32 v[22:23], v[22:23], v[62:63], v[50:51] op_sel_hi:[1,0,1]
	s_waitcnt vmcnt(1)
; __device__ __forceinline__ void ada_unit(KP Pk, Frame& F, int u) {
;     ...
; #pragma unroll
;         for (int q = 0; q < 16; ++q) {
; #pragma unroll
;             for (int r = 0; r < 9; ++r) a[r] += w[q] * sc[r * 128 + kh * 64 + k0 + q];
;             if ((q & 3) == 3) __builtin_amdgcn_sched_barrier(0); }
;     }
;     if (kh == 1) {
; #pragma unroll
;         for (int r = 0; r < 9; ++r) red[r * 256 + c4] = a[r]; }
	v_pk_fma_f32 v[50:51], v[10:11], v[12:13], v[56:57] op_sel:[0,1,0]
	v_pk_fma_f32 v[12:13], v[8:9], v[12:13], v[86:87] op_sel:[0,1,0]
	v_pk_fma_f32 v[56:57], v[10:11], v[16:17], v[94:95] op_sel:[0,1,0]
	v_pk_fma_f32 v[16:17], v[8:9], v[16:17], v[96:97] op_sel:[0,1,0]
	v_pk_fma_f32 v[66:67], v[10:11], v[24:25], v[66:67] op_sel:[0,1,0]
	v_pk_fma_f32 v[24:25], v[8:9], v[24:25], v[88:89] op_sel:[0,1,0]
	v_pk_fma_f32 v[68:69], v[10:11], v[28:29], v[68:69] op_sel:[0,1,0]
	v_pk_fma_f32 v[28:29], v[8:9], v[28:29], v[90:91] op_sel:[0,1,0]
	v_pk_fma_f32 v[70:71], v[10:11], v[32:33], v[70:71] op_sel:[0,1,0]
	v_pk_fma_f32 v[32:33], v[8:9], v[32:33], v[92:93] op_sel:[0,1,0]
	v_pk_fma_f32 v[42:43], v[10:11], v[36:37], v[42:43] op_sel:[0,1,0]
	v_pk_fma_f32 v[36:37], v[8:9], v[36:37], v[40:41] op_sel:[0,1,0]
	v_pk_fma_f32 v[44:45], v[8:9], v[46:47], v[44:45] op_sel:[0,1,0]
	v_pk_fma_f32 v[52:53], v[8:9], v[58:59], v[52:53] op_sel:[0,1,0]
	v_pk_fma_f32 v[8:9], v[8:9], v[62:63], v[20:21] op_sel:[0,1,0]
	v_pk_fma_f32 v[40:41], v[10:11], v[46:47], v[72:73] op_sel:[0,1,0]
	s_waitcnt vmcnt(0)
	v_pk_fma_f32 v[20:21], v[6:7], v[14:15], v[50:51] op_sel_hi:[1,0,1]
	v_pk_fma_f32 v[12:13], v[4:5], v[14:15], v[12:13] op_sel_hi:[1,0,1]
	v_pk_fma_f32 v[16:17], v[4:5], v[18:19], v[16:17] op_sel_hi:[1,0,1]
	v_pk_fma_f32 v[24:25], v[4:5], v[26:27], v[24:25] op_sel_hi:[1,0,1]
	v_pk_fma_f32 v[28:29], v[4:5], v[30:31], v[28:29] op_sel_hi:[1,0,1]
	v_pk_fma_f32 v[32:33], v[4:5], v[34:35], v[32:33] op_sel_hi:[1,0,1]
	v_pk_fma_f32 v[36:37], v[4:5], v[38:39], v[36:37] op_sel_hi:[1,0,1]
	v_pk_fma_f32 v[72:73], v[4:5], v[48:49], v[44:45] op_sel_hi:[1,0,1]
	v_pk_fma_f32 v[86:87], v[4:5], v[60:61], v[52:53] op_sel_hi:[1,0,1]
	v_pk_fma_f32 v[4:5], v[4:5], v[64:65], v[8:9] op_sel_hi:[1,0,1]
	v_mov_b32_e32 v8, v15
	v_pk_fma_f32 v[46:47], v[10:11], v[58:59], v[54:55] op_sel:[0,1,0]
	v_pk_fma_f32 v[10:11], v[10:11], v[62:63], v[22:23] op_sel:[0,1,0]
	v_pk_fma_f32 v[22:23], v[6:7], v[18:19], v[56:57] op_sel_hi:[1,0,1]
	v_pk_fma_f32 v[58:59], v[2:3], v[8:9], v[20:21] op_sel_hi:[1,0,1]
	v_pk_fma_f32 v[56:57], v[0:1], v[8:9], v[12:13] op_sel_hi:[1,0,1]
	v_mov_b32_e32 v8, v19
	v_pk_fma_f32 v[50:51], v[6:7], v[26:27], v[66:67] op_sel_hi:[1,0,1]
	v_pk_fma_f32 v[54:55], v[2:3], v[8:9], v[22:23] op_sel_hi:[1,0,1]
	v_pk_fma_f32 v[52:53], v[0:1], v[8:9], v[16:17] op_sel_hi:[1,0,1]
	v_mov_b32_e32 v8, v27
	v_pk_fma_f32 v[62:63], v[6:7], v[30:31], v[68:69] op_sel_hi:[1,0,1]
	v_pk_fma_f32 v[74:75], v[6:7], v[60:61], v[46:47] op_sel_hi:[1,0,1]
	v_pk_fma_f32 v[46:47], v[2:3], v[8:9], v[50:51] op_sel_hi:[1,0,1]
	v_pk_fma_f32 v[44:45], v[0:1], v[8:9], v[24:25] op_sel_hi:[1,0,1]
	v_mov_b32_e32 v8, v31
	v_pk_fma_f32 v[66:67], v[6:7], v[34:35], v[70:71] op_sel_hi:[1,0,1]
	v_pk_fma_f32 v[68:69], v[6:7], v[38:39], v[42:43] op_sel_hi:[1,0,1]
	v_pk_fma_f32 v[70:71], v[6:7], v[48:49], v[40:41] op_sel_hi:[1,0,1]
	v_pk_fma_f32 v[42:43], v[2:3], v[8:9], v[62:63] op_sel_hi:[1,0,1]
	v_pk_fma_f32 v[40:41], v[0:1], v[8:9], v[28:29] op_sel_hi:[1,0,1]
	v_mov_b32_e32 v8, v35
	v_pk_fma_f32 v[34:35], v[2:3], v[8:9], v[66:67] op_sel_hi:[1,0,1]
	v_pk_fma_f32 v[32:33], v[0:1], v[8:9], v[32:33] op_sel_hi:[1,0,1]
	v_mov_b32_e32 v8, v39
	v_pk_fma_f32 v[30:31], v[2:3], v[8:9], v[68:69] op_sel_hi:[1,0,1]
	v_pk_fma_f32 v[28:29], v[0:1], v[8:9], v[36:37] op_sel_hi:[1,0,1]
	v_mov_b32_e32 v8, v49
	v_pk_fma_f32 v[26:27], v[2:3], v[8:9], v[70:71] op_sel_hi:[1,0,1]
	v_pk_fma_f32 v[24:25], v[0:1], v[8:9], v[72:73] op_sel_hi:[1,0,1]
	v_mov_b32_e32 v8, v61
	v_pk_fma_f32 v[6:7], v[6:7], v[64:65], v[10:11] op_sel_hi:[1,0,1]
	v_pk_fma_f32 v[18:19], v[2:3], v[8:9], v[74:75] op_sel_hi:[1,0,1]
	v_pk_fma_f32 v[16:17], v[0:1], v[8:9], v[86:87] op_sel_hi:[1,0,1]
	v_mov_b32_e32 v8, v65
	v_pk_fma_f32 v[14:15], v[2:3], v[8:9], v[6:7] op_sel_hi:[1,0,1]
	v_pk_fma_f32 v[12:13], v[0:1], v[8:9], v[4:5] op_sel_hi:[1,0,1]
	s_add_i32 s23, s23, 16
	s_add_i32 s28, s28, 64
	s_cmp_gt_u32 s23, 47
	v_lshl_add_u64 v[78:79], v[78:79], 0, s[18:19]
	s_cbranch_scc0 .LBB0_95
	s_andn2_b64 vcc, exec, s[6:7]
	s_cbranch_vccnz .LBB0_98
	v_lshl_add_u32 v0, v85, 4, 0
	ds_write_b128 v0, v[56:59] offset:4608
	ds_write_b128 v0, v[52:55] offset:8704
	ds_write_b128 v0, v[44:47] offset:12800
	ds_write_b128 v0, v[40:43] offset:16896
	ds_write_b128 v0, v[32:35] offset:20992
	ds_write_b128 v0, v[28:31] offset:25088
	ds_write_b128 v0, v[24:27] offset:29184
	ds_write_b128 v0, v[16:19] offset:33280
	ds_write_b128 v0, v[12:15] offset:37376

; __device__ __forceinline__ void ada_unit(KP Pk, Frame& F, int u) {
;     ...
;     if ((F.MISC[1] & 15u) == 15u) {
;         __builtin_amdgcn_fence(__ATOMIC_ACQUIRE, "agent");
;         for (int i = F.tid; i < 9 * 256; i += NTHR) { const int r = i >> 8, cc = i & 255;
;             f32x4 sum = *(const f32x4*)(Pk->in[I_ADAB] + l * 12288 + cb * 1024 + 4 * cc), pv[16];
; #pragma unroll
;             for (int k2 = 0; k2 < 16; ++k2) pv[k2] = *(const f32x4*)(part + ((size_t)((l * 16 + k2) * 9 + r)) * 12288 + cb * 1024 + 4 * cc);
; #pragma unroll
;             for (int k2 = 0; k2 < 16; ++k2) sum += pv[k2];
;             *(f32x4*)((float*)(ws + WS_MOD) + ((size_t)l * 9 + r) * 12288 + cb * 1024 + 4 * cc) = sum; } }
.LBB0_107:
	v_and_b32_e32 v2, 0x3fc, v0
	v_lshlrev_b32_e32 v76, 2, v2
	global_load_dwordx4 v[2:5], v76, s[30:31] nt
	v_ashrrev_i32_e32 v70, 8, v1
	v_add_u32_e32 v8, s4, v70
	v_add_u32_e32 v10, s78, v70
	v_lshl_add_u64 v[6:7], s[34:35], 0, v[76:77]
	v_add_u32_e32 v12, 18, v8
	v_add_u32_e32 v13, 27, v8
	v_add_u32_e32 v16, 36, v8
	v_add_u32_e32 v17, 45, v8
	v_add_u32_e32 v20, 54, v8
	v_add_u32_e32 v21, 63, v8
	v_add_u32_e32 v24, 0x48, v8
	v_add_u32_e32 v25, 0x51, v8
	v_add_u32_e32 v28, 0x5a, v8
	v_add_u32_e32 v29, 0x63, v8
	v_add_u32_e32 v32, 0x6c, v8
	v_add_u32_e32 v33, 0x75, v8
	v_add_u32_e32 v36, 0x7e, v8
	v_add_u32_e32 v37, 0x87, v8
	v_mad_i64_i32 v[8:9], s[80:81], v8, s59, v[6:7]
	v_mad_i64_i32 v[10:11], s[80:81], v10, s59, v[6:7]
	v_mad_i64_i32 v[14:15], s[80:81], v12, s59, v[6:7]
	v_mad_i64_i32 v[18:19], s[80:81], v13, s59, v[6:7]
	v_mad_i64_i32 v[22:23], s[80:81], v16, s59, v[6:7]
	v_mad_i64_i32 v[26:27], s[80:81], v17, s59, v[6:7]
	v_mad_i64_i32 v[30:31], s[80:81], v20, s59, v[6:7]
	v_mad_i64_i32 v[34:35], s[80:81], v21, s59, v[6:7]
	v_mad_i64_i32 v[38:39], s[80:81], v24, s59, v[6:7]
	v_mad_i64_i32 v[42:43], s[80:81], v25, s59, v[6:7]
	v_mad_i64_i32 v[46:47], s[80:81], v28, s59, v[6:7]
	v_mad_i64_i32 v[50:51], s[80:81], v29, s59, v[6:7]
	v_mad_i64_i32 v[54:55], s[80:81], v32, s59, v[6:7]
	v_mad_i64_i32 v[58:59], s[80:81], v33, s59, v[6:7]
	v_mad_i64_i32 v[62:63], s[80:81], v36, s59, v[6:7]
	v_mad_i64_i32 v[66:67], s[80:81], v37, s59, v[6:7]
	global_load_dwordx4 v[6:9], v[8:9], off nt
	s_nop 0
	global_load_dwordx4 v[10:13], v[10:11], off nt
	s_nop 0
	global_load_dwordx4 v[14:17], v[14:15], off nt
	s_nop 0
	global_load_dwordx4 v[18:21], v[18:19], off nt
	s_nop 0
	global_load_dwordx4 v[22:25], v[22:23], off nt
	s_nop 0
	global_load_dwordx4 v[26:29], v[26:27], off nt
	s_nop 0
	global_load_dwordx4 v[30:33], v[30:31], off nt
	s_nop 0
	global_load_dwordx4 v[34:37], v[34:35], off nt
	s_nop 0
	global_load_dwordx4 v[38:41], v[38:39], off nt
	s_nop 0
	global_load_dwordx4 v[42:45], v[42:43], off nt
	s_nop 0
	global_load_dwordx4 v[46:49], v[46:47], off nt
	s_nop 0
	global_load_dwordx4 v[50:53], v[50:51], off nt
	s_nop 0
	global_load_dwordx4 v[54:57], v[54:55], off nt
	s_nop 0
	global_load_dwordx4 v[58:61], v[58:59], off nt
	s_nop 0
	global_load_dwordx4 v[62:65], v[62:63], off nt
	s_nop 0
	global_load_dwordx4 v[66:69], v[66:67], off nt
	v_ashrrev_i32_e32 v71, 31, v70
	v_mov_b64_e32 v[72:73], s[20:21]
	v_lshl_add_u64 v[70:71], s[28:29], 0, v[70:71]
	v_mad_u64_u32 v[72:73], s[80:81], v70, s59, v[72:73]
	v_mov_b32_e32 v70, v73
	v_mad_u64_u32 v[70:71], s[80:81], v71, s59, v[70:71]
	v_add_u32_e32 v74, 0x200, v1
	v_cmp_lt_i32_e32 vcc, s77, v1
	v_mov_b32_e32 v73, v70
	v_add_u32_e32 v0, 0x800, v0
	s_or_b64 s[36:37], vcc, s[36:37]
	v_mov_b32_e32 v1, v74
	v_lshl_add_u64 v[70:71], v[72:73], 0, v[76:77]
	s_waitcnt vmcnt(15)
	v_pk_add_f32 v[4:5], v[4:5], v[8:9]
	v_pk_add_f32 v[2:3], v[2:3], v[6:7]
	s_waitcnt vmcnt(14)
	v_pk_add_f32 v[4:5], v[4:5], v[12:13]
	v_pk_add_f32 v[2:3], v[2:3], v[10:11]
	s_waitcnt vmcnt(13)
	v_pk_add_f32 v[4:5], v[4:5], v[16:17]
	v_pk_add_f32 v[2:3], v[2:3], v[14:15]
	s_waitcnt vmcnt(12)
	v_pk_add_f32 v[4:5], v[4:5], v[20:21]
	v_pk_add_f32 v[2:3], v[2:3], v[18:19]
	s_waitcnt vmcnt(11)
	v_pk_add_f32 v[4:5], v[4:5], v[24:25]
	v_pk_add_f32 v[2:3], v[2:3], v[22:23]
	s_waitcnt vmcnt(10)
	v_pk_add_f32 v[4:5], v[4:5], v[28:29]
	v_pk_add_f32 v[2:3], v[2:3], v[26:27]
	s_waitcnt vmcnt(9)
	v_pk_add_f32 v[4:5], v[4:5], v[32:33]
	v_pk_add_f32 v[2:3], v[2:3], v[30:31]
	s_waitcnt vmcnt(8)
	v_pk_add_f32 v[4:5], v[4:5], v[36:37]
	v_pk_add_f32 v[2:3], v[2:3], v[34:35]
	s_waitcnt vmcnt(7)
	v_pk_add_f32 v[4:5], v[4:5], v[40:41]
	v_pk_add_f32 v[2:3], v[2:3], v[38:39]
	s_waitcnt vmcnt(6)
	v_pk_add_f32 v[4:5], v[4:5], v[44:45]
	v_pk_add_f32 v[2:3], v[2:3], v[42:43]
	s_waitcnt vmcnt(5)
	v_pk_add_f32 v[4:5], v[4:5], v[48:49]
	v_pk_add_f32 v[2:3], v[2:3], v[46:47]
	s_waitcnt vmcnt(4)
	v_pk_add_f32 v[4:5], v[4:5], v[52:53]
	v_pk_add_f32 v[2:3], v[2:3], v[50:51]
	s_waitcnt vmcnt(3)
	v_pk_add_f32 v[4:5], v[4:5], v[56:57]
	v_pk_add_f32 v[2:3], v[2:3], v[54:55]
	s_waitcnt vmcnt(2)
	v_pk_add_f32 v[4:5], v[4:5], v[60:61]
	v_pk_add_f32 v[2:3], v[2:3], v[58:59]
	s_waitcnt vmcnt(1)
	v_pk_add_f32 v[4:5], v[4:5], v[64:65]
	v_pk_add_f32 v[2:3], v[2:3], v[62:63]
	s_waitcnt vmcnt(0)
	v_pk_add_f32 v[4:5], v[4:5], v[68:69]
	v_pk_add_f32 v[2:3], v[2:3], v[66:67]
	global_store_dwordx4 v[70:71], v[2:5], off
	s_andn2_b64 exec, exec, s[36:37]
	s_cbranch_execnz .LBB0_107
	s_branch .LBB0_61

; __device__ __forceinline__ void ada_unit(KP Pk, Frame& F, int u) {
;     ...
; #pragma unroll 1
;     for (int k0 = 0; k0 < 64; k0 += 16) {
;         f32x4 w[16];
; #pragma unroll
;         for (int q = 0; q < 16; ++q) w[q] = W[(size_t)(k0 + q) * 3072];
; #pragma unroll
;         for (int q = 0; q < 16; ++q) {
; #pragma unroll
;             for (int r = 0; r < 9; ++r) a[r] += w[q] * sc[r * 128 + kh * 64 + k0 + q];
;             if ((q & 3) == 3) __builtin_amdgcn_sched_barrier(0); }
.LBB0_574:
	s_mov_b32 s18, 0xfff4c000
	v_add_co_u32_e32 v22, vcc, s18, v86
	s_mov_b32 s18, 0xfff58000
	s_nop 0
	v_addc_co_u32_e32 v23, vcc, -1, v87, vcc
	global_load_dwordx4 v[90:93], v[22:23], off nt
	v_add_co_u32_e32 v22, vcc, s18, v86
	s_mov_b32 s18, 0xfff64000
	s_nop 0
	v_addc_co_u32_e32 v23, vcc, -1, v87, vcc
	v_add_co_u32_e32 v24, vcc, s18, v86
	s_mov_b32 s18, 0xfff70000
	s_nop 0
	v_addc_co_u32_e32 v25, vcc, -1, v87, vcc
	v_add_co_u32_e32 v38, vcc, s18, v86
	s_mov_b32 s18, 0xfff7c000
	s_nop 0
	v_addc_co_u32_e32 v39, vcc, -1, v87, vcc
	v_add_co_u32_e32 v40, vcc, s18, v86
	s_mov_b32 s18, 0xfff88000
	s_nop 0
	v_addc_co_u32_e32 v41, vcc, -1, v87, vcc
	v_add_co_u32_e32 v42, vcc, s18, v86
	s_mov_b32 s18, 0xfff94000
	s_nop 0
	v_addc_co_u32_e32 v43, vcc, -1, v87, vcc
	v_add_co_u32_e32 v44, vcc, s18, v86
	s_mov_b32 s18, 0xfffa0000
	s_nop 0
	v_addc_co_u32_e32 v45, vcc, -1, v87, vcc
	v_add_co_u32_e32 v46, vcc, s18, v86
	s_mov_b32 s18, 0xfffac000
	s_nop 0
	v_addc_co_u32_e32 v47, vcc, -1, v87, vcc
	v_add_co_u32_e32 v48, vcc, s18, v86
	s_mov_b32 s18, 0xfffb8000
	s_nop 0
	v_addc_co_u32_e32 v49, vcc, -1, v87, vcc
	v_add_co_u32_e32 v54, vcc, s18, v86
	global_load_dwordx4 v[94:97], v[22:23], off nt
	global_load_dwordx4 v[98:101], v[24:25], off nt
	v_addc_co_u32_e32 v55, vcc, -1, v87, vcc
	s_mov_b32 s18, 0xfffc4000
	v_add_co_u32_e32 v56, vcc, s18, v86
	s_mov_b32 s18, 0xfffd0000
	s_nop 0
	v_addc_co_u32_e32 v57, vcc, -1, v87, vcc
	global_load_dwordx4 v[102:105], v[38:39], off nt
	global_load_dwordx4 v[22:25], v[86:87], off nt
	v_add_co_u32_e32 v106, vcc, s18, v86
	s_mov_b32 s18, 0xfffdc000
	s_nop 0
	v_addc_co_u32_e32 v107, vcc, -1, v87, vcc
	global_load_dwordx4 v[82:85], v[40:41], off nt
	global_load_dwordx4 v[78:81], v[42:43], off nt
	global_load_dwordx4 v[74:77], v[44:45], off nt
	global_load_dwordx4 v[70:73], v[46:47], off nt
	global_load_dwordx4 v[66:69], v[48:49], off nt
	global_load_dwordx4 v[62:65], v[54:55], off nt
	global_load_dwordx4 v[58:61], v[56:57], off nt
	s_nop 0
	global_load_dwordx4 v[54:57], v[106:107], off nt
	v_add_co_u32_e32 v110, vcc, s18, v86
	s_mov_b32 s18, 0xfffe8000
	s_nop 0
	v_addc_co_u32_e32 v111, vcc, -1, v87, vcc
	v_add_co_u32_e32 v112, vcc, s18, v86
	s_mov_b32 s18, 0xffff4000
	s_nop 0
	v_addc_co_u32_e32 v113, vcc, -1, v87, vcc
	v_add_co_u32_e32 v38, vcc, s18, v86
	v_mov_b32_e32 v88, s9
	s_nop 0
	v_addc_co_u32_e32 v39, vcc, -1, v87, vcc
	ds_read_b128 v[106:109], v88
	global_load_dwordx4 v[46:49], v[110:111], off nt
	global_load_dwordx4 v[42:45], v[112:113], off nt
	ds_read_b128 v[110:113], v88 offset:512
	ds_read_b128 v[114:117], v88 offset:1024
	global_load_dwordx4 v[38:41], v[38:39], off nt
	s_waitcnt vmcnt(15) lgkmcnt(2)
	v_pk_fma_f32 v[122:123], v[92:93], v[106:107], v[52:53] op_sel_hi:[1,0,1]
	v_pk_fma_f32 v[124:125], v[90:91], v[106:107], v[50:51] op_sel_hi:[1,0,1]
	ds_read_b128 v[50:53], v88 offset:1536
	s_waitcnt lgkmcnt(2)
	v_pk_fma_f32 v[126:127], v[90:91], v[110:111], v[34:35] op_sel_hi:[1,0,1]
	s_waitcnt lgkmcnt(1)
	v_pk_fma_f32 v[128:129], v[92:93], v[114:115], v[32:33] op_sel_hi:[1,0,1]
	ds_read_b128 v[32:35], v88 offset:2048
	v_pk_fma_f32 v[130:131], v[90:91], v[114:115], v[30:31] op_sel_hi:[1,0,1]
	s_waitcnt lgkmcnt(1)
	v_pk_fma_f32 v[132:133], v[92:93], v[50:51], v[28:29] op_sel_hi:[1,0,1]
	ds_read_b128 v[28:31], v88 offset:2560
	ds_read_b128 v[118:121], v88 offset:3584
	s_waitcnt lgkmcnt(2)
	v_pk_fma_f32 v[134:135], v[92:93], v[32:33], v[20:21] op_sel_hi:[1,0,1]
	v_pk_fma_f32 v[136:137], v[90:91], v[32:33], v[18:19] op_sel_hi:[1,0,1]
	ds_read_b128 v[18:21], v88 offset:3072
	s_waitcnt lgkmcnt(2)
	v_pk_fma_f32 v[138:139], v[92:93], v[28:29], v[16:17] op_sel_hi:[1,0,1]
	v_pk_fma_f32 v[140:141], v[90:91], v[28:29], v[14:15] op_sel_hi:[1,0,1]
	ds_read_b128 v[14:17], v88 offset:4096
	v_pk_fma_f32 v[36:37], v[92:93], v[110:111], v[36:37] op_sel_hi:[1,0,1]
	v_pk_fma_f32 v[26:27], v[90:91], v[50:51], v[26:27] op_sel_hi:[1,0,1]
	s_waitcnt lgkmcnt(1)
	v_pk_fma_f32 v[12:13], v[92:93], v[18:19], v[12:13] op_sel_hi:[1,0,1]
	v_pk_fma_f32 v[10:11], v[90:91], v[18:19], v[10:11] op_sel_hi:[1,0,1]
	s_waitcnt lgkmcnt(0)
	v_pk_fma_f32 v[4:5], v[92:93], v[14:15], v[4:5] op_sel_hi:[1,0,1]
	v_pk_fma_f32 v[2:3], v[90:91], v[14:15], v[2:3] op_sel_hi:[1,0,1]
	v_pk_fma_f32 v[8:9], v[92:93], v[118:119], v[8:9] op_sel_hi:[1,0,1]
	v_pk_fma_f32 v[6:7], v[90:91], v[118:119], v[6:7] op_sel_hi:[1,0,1]
	s_waitcnt vmcnt(14)
	v_pk_fma_f32 v[90:91], v[96:97], v[106:107], v[122:123] op_sel:[0,1,0]
	v_pk_fma_f32 v[92:93], v[94:95], v[106:107], v[124:125] op_sel:[0,1,0]
	v_pk_fma_f32 v[4:5], v[96:97], v[14:15], v[4:5] op_sel:[0,1,0]
	v_pk_fma_f32 v[2:3], v[94:95], v[14:15], v[2:3] op_sel:[0,1,0]
	v_pk_fma_f32 v[36:37], v[96:97], v[110:111], v[36:37] op_sel:[0,1,0]
	v_pk_fma_f32 v[106:107], v[94:95], v[110:111], v[126:127] op_sel:[0,1,0]
	v_pk_fma_f32 v[12:13], v[96:97], v[18:19], v[12:13] op_sel:[0,1,0]
	v_pk_fma_f32 v[10:11], v[94:95], v[18:19], v[10:11] op_sel:[0,1,0]
	s_waitcnt vmcnt(13)
	v_pk_fma_f32 v[14:15], v[100:101], v[108:109], v[90:91] op_sel_hi:[1,0,1]
	v_pk_fma_f32 v[18:19], v[98:99], v[108:109], v[92:93] op_sel_hi:[1,0,1]
	v_pk_fma_f32 v[4:5], v[100:101], v[16:17], v[4:5] op_sel_hi:[1,0,1]
	v_pk_fma_f32 v[2:3], v[98:99], v[16:17], v[2:3] op_sel_hi:[1,0,1]
	v_mov_b32_e32 v16, v109
	v_pk_fma_f32 v[110:111], v[96:97], v[114:115], v[128:129] op_sel:[0,1,0]
	v_pk_fma_f32 v[114:115], v[94:95], v[114:115], v[130:131] op_sel:[0,1,0]
	v_pk_fma_f32 v[36:37], v[100:101], v[112:113], v[36:37] op_sel_hi:[1,0,1]
	v_pk_fma_f32 v[90:91], v[98:99], v[112:113], v[106:107] op_sel_hi:[1,0,1]
	s_waitcnt vmcnt(12)
; __device__ __forceinline__ void ada_unit(KP Pk, Frame& F, int u) {
;     ...
; #pragma unroll
;         for (int q = 0; q < 16; ++q) {
; #pragma unroll
;             for (int r = 0; r < 9; ++r) a[r] += w[q] * sc[r * 128 + kh * 64 + k0 + q];
;             if ((q & 3) == 3) __builtin_amdgcn_sched_barrier(0); }
	v_pk_fma_f32 v[14:15], v[104:105], v[16:17], v[14:15] op_sel_hi:[1,0,1]
	v_pk_fma_f32 v[18:19], v[102:103], v[16:17], v[18:19] op_sel_hi:[1,0,1]
	v_mov_b32_e32 v16, v113
	v_pk_fma_f32 v[122:123], v[96:97], v[50:51], v[132:133] op_sel:[0,1,0]
	v_pk_fma_f32 v[26:27], v[94:95], v[50:51], v[26:27] op_sel:[0,1,0]
	v_pk_fma_f32 v[50:51], v[96:97], v[32:33], v[134:135] op_sel:[0,1,0]
	v_pk_fma_f32 v[32:33], v[94:95], v[32:33], v[136:137] op_sel:[0,1,0]
	v_pk_fma_f32 v[124:125], v[96:97], v[28:29], v[138:139] op_sel:[0,1,0]
	v_pk_fma_f32 v[28:29], v[94:95], v[28:29], v[140:141] op_sel:[0,1,0]
	v_pk_fma_f32 v[6:7], v[94:95], v[118:119], v[6:7] op_sel:[0,1,0]
	v_pk_fma_f32 v[92:93], v[100:101], v[116:117], v[110:111] op_sel_hi:[1,0,1]
	v_pk_fma_f32 v[94:95], v[98:99], v[116:117], v[114:115] op_sel_hi:[1,0,1]
	v_pk_fma_f32 v[36:37], v[104:105], v[16:17], v[36:37] op_sel_hi:[1,0,1]
	v_pk_fma_f32 v[90:91], v[102:103], v[16:17], v[90:91] op_sel_hi:[1,0,1]
	v_mov_b32_e32 v16, v117
	v_pk_fma_f32 v[8:9], v[96:97], v[118:119], v[8:9] op_sel:[0,1,0]
	v_pk_fma_f32 v[96:97], v[100:101], v[52:53], v[122:123] op_sel_hi:[1,0,1]
	v_pk_fma_f32 v[26:27], v[98:99], v[52:53], v[26:27] op_sel_hi:[1,0,1]
	v_pk_fma_f32 v[92:93], v[104:105], v[16:17], v[92:93] op_sel_hi:[1,0,1]
	v_pk_fma_f32 v[94:95], v[102:103], v[16:17], v[94:95] op_sel_hi:[1,0,1]
	v_mov_b32_e32 v16, v53
	v_pk_fma_f32 v[50:51], v[100:101], v[34:35], v[50:51] op_sel_hi:[1,0,1]
	v_pk_fma_f32 v[32:33], v[98:99], v[34:35], v[32:33] op_sel_hi:[1,0,1]
	v_pk_fma_f32 v[52:53], v[104:105], v[16:17], v[96:97] op_sel_hi:[1,0,1]
	v_pk_fma_f32 v[96:97], v[102:103], v[16:17], v[26:27] op_sel_hi:[1,0,1]
	v_mov_b32_e32 v16, v35
	v_pk_fma_f32 v[106:107], v[100:101], v[30:31], v[124:125] op_sel_hi:[1,0,1]
	v_pk_fma_f32 v[28:29], v[98:99], v[30:31], v[28:29] op_sel_hi:[1,0,1]
	v_pk_fma_f32 v[34:35], v[104:105], v[16:17], v[50:51] op_sel_hi:[1,0,1]
	v_pk_fma_f32 v[32:33], v[102:103], v[16:17], v[32:33] op_sel_hi:[1,0,1]
	v_mov_b32_e32 v16, v31
	v_pk_fma_f32 v[10:11], v[98:99], v[20:21], v[10:11] op_sel_hi:[1,0,1]
	v_pk_fma_f32 v[6:7], v[98:99], v[120:121], v[6:7] op_sel_hi:[1,0,1]
	v_pk_fma_f32 v[50:51], v[104:105], v[16:17], v[106:107] op_sel_hi:[1,0,1]
	v_pk_fma_f32 v[98:99], v[102:103], v[16:17], v[28:29] op_sel_hi:[1,0,1]
	v_mov_b32_e32 v16, v21
	v_pk_fma_f32 v[106:107], v[102:103], v[16:17], v[10:11] op_sel_hi:[1,0,1]
	v_mov_b32_e32 v10, v121
	v_pk_fma_f32 v[12:13], v[100:101], v[20:21], v[12:13] op_sel_hi:[1,0,1]
	v_pk_fma_f32 v[8:9], v[100:101], v[120:121], v[8:9] op_sel_hi:[1,0,1]
	v_pk_fma_f32 v[110:111], v[102:103], v[10:11], v[6:7] op_sel_hi:[1,0,1]
	v_mov_b32_e32 v6, v17
	v_pk_fma_f32 v[100:101], v[104:105], v[16:17], v[12:13] op_sel_hi:[1,0,1]
	v_pk_fma_f32 v[108:109], v[104:105], v[10:11], v[8:9] op_sel_hi:[1,0,1]
	v_pk_fma_f32 v[104:105], v[104:105], v[6:7], v[4:5] op_sel_hi:[1,0,1]
	v_pk_fma_f32 v[102:103], v[102:103], v[6:7], v[2:3] op_sel_hi:[1,0,1]
	ds_read_b128 v[2:5], v88 offset:16
	ds_read_b128 v[6:9], v88 offset:528
	ds_read_b128 v[10:13], v88 offset:1040
	ds_read_b128 v[26:29], v88 offset:2576
	s_waitcnt vmcnt(10) lgkmcnt(3)
	v_pk_fma_f32 v[112:113], v[84:85], v[2:3], v[14:15] op_sel_hi:[1,0,1]
	v_pk_fma_f32 v[114:115], v[82:83], v[2:3], v[18:19] op_sel_hi:[1,0,1]
	ds_read_b128 v[14:17], v88 offset:1552
	ds_read_b128 v[18:21], v88 offset:2064
	s_waitcnt lgkmcnt(4)
	v_pk_fma_f32 v[116:117], v[84:85], v[6:7], v[36:37] op_sel_hi:[1,0,1]
	v_pk_fma_f32 v[90:91], v[82:83], v[6:7], v[90:91] op_sel_hi:[1,0,1]
	s_waitcnt lgkmcnt(3)
	v_pk_fma_f32 v[92:93], v[84:85], v[10:11], v[92:93] op_sel_hi:[1,0,1]
	s_waitcnt lgkmcnt(1)
	v_pk_fma_f32 v[118:119], v[84:85], v[14:15], v[52:53] op_sel_hi:[1,0,1]
	s_waitcnt lgkmcnt(0)
	v_pk_fma_f32 v[120:121], v[84:85], v[18:19], v[34:35] op_sel_hi:[1,0,1]
	v_pk_fma_f32 v[122:123], v[82:83], v[18:19], v[32:33] op_sel_hi:[1,0,1]
	ds_read_b128 v[30:33], v88 offset:3088
	v_pk_fma_f32 v[124:125], v[84:85], v[26:27], v[50:51] op_sel_hi:[1,0,1]
	ds_read_b128 v[34:37], v88 offset:3600
	ds_read_b128 v[50:53], v88 offset:4112
	v_pk_fma_f32 v[94:95], v[82:83], v[10:11], v[94:95] op_sel_hi:[1,0,1]
	v_pk_fma_f32 v[96:97], v[82:83], v[14:15], v[96:97] op_sel_hi:[1,0,1]
	v_pk_fma_f32 v[98:99], v[82:83], v[26:27], v[98:99] op_sel_hi:[1,0,1]
	s_waitcnt lgkmcnt(2)
	v_pk_fma_f32 v[100:101], v[84:85], v[30:31], v[100:101] op_sel_hi:[1,0,1]
	v_pk_fma_f32 v[106:107], v[82:83], v[30:31], v[106:107] op_sel_hi:[1,0,1]
	s_waitcnt lgkmcnt(1)
	v_pk_fma_f32 v[108:109], v[84:85], v[34:35], v[108:109] op_sel_hi:[1,0,1]
	v_pk_fma_f32 v[110:111], v[82:83], v[34:35], v[110:111] op_sel_hi:[1,0,1]
	s_waitcnt lgkmcnt(0)
	v_pk_fma_f32 v[84:85], v[84:85], v[50:51], v[104:105] op_sel_hi:[1,0,1]
	v_pk_fma_f32 v[82:83], v[82:83], v[50:51], v[102:103] op_sel_hi:[1,0,1]
	s_waitcnt vmcnt(9)
	v_pk_fma_f32 v[102:103], v[80:81], v[2:3], v[112:113] op_sel:[0,1,0]
	v_pk_fma_f32 v[2:3], v[78:79], v[2:3], v[114:115] op_sel:[0,1,0]
	v_pk_fma_f32 v[104:105], v[80:81], v[6:7], v[116:117] op_sel:[0,1,0]
	v_pk_fma_f32 v[6:7], v[78:79], v[6:7], v[90:91] op_sel:[0,1,0]
	v_pk_fma_f32 v[90:91], v[80:81], v[10:11], v[92:93] op_sel:[0,1,0]
	v_pk_fma_f32 v[10:11], v[78:79], v[10:11], v[94:95] op_sel:[0,1,0]
	v_pk_fma_f32 v[92:93], v[80:81], v[14:15], v[118:119] op_sel:[0,1,0]
	v_pk_fma_f32 v[14:15], v[78:79], v[14:15], v[96:97] op_sel:[0,1,0]
	v_pk_fma_f32 v[94:95], v[80:81], v[18:19], v[120:121] op_sel:[0,1,0]
	v_pk_fma_f32 v[18:19], v[78:79], v[18:19], v[122:123] op_sel:[0,1,0]
	v_pk_fma_f32 v[96:97], v[80:81], v[26:27], v[124:125] op_sel:[0,1,0]
	v_pk_fma_f32 v[26:27], v[78:79], v[26:27], v[98:99] op_sel:[0,1,0]
	v_pk_fma_f32 v[98:99], v[80:81], v[30:31], v[100:101] op_sel:[0,1,0]
	v_pk_fma_f32 v[30:31], v[78:79], v[30:31], v[106:107] op_sel:[0,1,0]
	v_pk_fma_f32 v[100:101], v[80:81], v[34:35], v[108:109] op_sel:[0,1,0]
	v_pk_fma_f32 v[34:35], v[78:79], v[34:35], v[110:111] op_sel:[0,1,0]
	v_pk_fma_f32 v[80:81], v[80:81], v[50:51], v[84:85] op_sel:[0,1,0]
	v_pk_fma_f32 v[50:51], v[78:79], v[50:51], v[82:83] op_sel:[0,1,0]
	s_waitcnt vmcnt(8)
; __device__ __forceinline__ void ada_unit(KP Pk, Frame& F, int u) {
;     ...
; #pragma unroll
;         for (int q = 0; q < 16; ++q) {
; #pragma unroll
;             for (int r = 0; r < 9; ++r) a[r] += w[q] * sc[r * 128 + kh * 64 + k0 + q];
;             if ((q & 3) == 3) __builtin_amdgcn_sched_barrier(0); }
	v_pk_fma_f32 v[78:79], v[76:77], v[4:5], v[102:103] op_sel_hi:[1,0,1]
	v_pk_fma_f32 v[2:3], v[74:75], v[4:5], v[2:3] op_sel_hi:[1,0,1]
	v_mov_b32_e32 v4, v5
	v_pk_fma_f32 v[82:83], v[76:77], v[8:9], v[104:105] op_sel_hi:[1,0,1]
	v_pk_fma_f32 v[6:7], v[74:75], v[8:9], v[6:7] op_sel_hi:[1,0,1]
	v_pk_fma_f32 v[10:11], v[74:75], v[12:13], v[10:11] op_sel_hi:[1,0,1]
	v_pk_fma_f32 v[14:15], v[74:75], v[16:17], v[14:15] op_sel_hi:[1,0,1]
	v_pk_fma_f32 v[18:19], v[74:75], v[20:21], v[18:19] op_sel_hi:[1,0,1]
	v_pk_fma_f32 v[26:27], v[74:75], v[28:29], v[26:27] op_sel_hi:[1,0,1]
	v_pk_fma_f32 v[30:31], v[74:75], v[32:33], v[30:31] op_sel_hi:[1,0,1]
	v_pk_fma_f32 v[34:35], v[74:75], v[36:37], v[34:35] op_sel_hi:[1,0,1]
	v_pk_fma_f32 v[50:51], v[74:75], v[52:53], v[50:51] op_sel_hi:[1,0,1]
	s_waitcnt vmcnt(7)
	v_pk_fma_f32 v[74:75], v[72:73], v[4:5], v[78:79] op_sel_hi:[1,0,1]
	v_pk_fma_f32 v[78:79], v[70:71], v[4:5], v[2:3] op_sel_hi:[1,0,1]
	v_mov_b32_e32 v2, v9
	v_pk_fma_f32 v[84:85], v[76:77], v[12:13], v[90:91] op_sel_hi:[1,0,1]
	v_pk_fma_f32 v[90:91], v[76:77], v[16:17], v[92:93] op_sel_hi:[1,0,1]
	v_pk_fma_f32 v[92:93], v[76:77], v[20:21], v[94:95] op_sel_hi:[1,0,1]
	v_pk_fma_f32 v[94:95], v[76:77], v[28:29], v[96:97] op_sel_hi:[1,0,1]
	v_pk_fma_f32 v[96:97], v[76:77], v[32:33], v[98:99] op_sel_hi:[1,0,1]
	v_pk_fma_f32 v[98:99], v[76:77], v[36:37], v[100:101] op_sel_hi:[1,0,1]
	v_pk_fma_f32 v[76:77], v[76:77], v[52:53], v[80:81] op_sel_hi:[1,0,1]
	v_pk_fma_f32 v[80:81], v[72:73], v[2:3], v[82:83] op_sel_hi:[1,0,1]
	v_pk_fma_f32 v[82:83], v[70:71], v[2:3], v[6:7] op_sel_hi:[1,0,1]
	v_mov_b32_e32 v2, v13
	v_pk_fma_f32 v[84:85], v[72:73], v[2:3], v[84:85] op_sel_hi:[1,0,1]
	v_pk_fma_f32 v[100:101], v[70:71], v[2:3], v[10:11] op_sel_hi:[1,0,1]
	v_mov_b32_e32 v2, v17
	v_pk_fma_f32 v[90:91], v[72:73], v[2:3], v[90:91] op_sel_hi:[1,0,1]
	v_pk_fma_f32 v[102:103], v[70:71], v[2:3], v[14:15] op_sel_hi:[1,0,1]
	v_mov_b32_e32 v2, v21
	v_pk_fma_f32 v[92:93], v[72:73], v[2:3], v[92:93] op_sel_hi:[1,0,1]
	v_pk_fma_f32 v[104:105], v[70:71], v[2:3], v[18:19] op_sel_hi:[1,0,1]
	v_mov_b32_e32 v2, v29
	v_pk_fma_f32 v[94:95], v[72:73], v[2:3], v[94:95] op_sel_hi:[1,0,1]
	v_pk_fma_f32 v[106:107], v[70:71], v[2:3], v[26:27] op_sel_hi:[1,0,1]
	v_mov_b32_e32 v2, v33
	v_pk_fma_f32 v[96:97], v[72:73], v[2:3], v[96:97] op_sel_hi:[1,0,1]
	v_pk_fma_f32 v[108:109], v[70:71], v[2:3], v[30:31] op_sel_hi:[1,0,1]
	v_mov_b32_e32 v2, v37
	v_pk_fma_f32 v[98:99], v[72:73], v[2:3], v[98:99] op_sel_hi:[1,0,1]
	v_pk_fma_f32 v[110:111], v[70:71], v[2:3], v[34:35] op_sel_hi:[1,0,1]
	v_mov_b32_e32 v2, v53
	v_pk_fma_f32 v[72:73], v[72:73], v[2:3], v[76:77] op_sel_hi:[1,0,1]
	v_pk_fma_f32 v[70:71], v[70:71], v[2:3], v[50:51] op_sel_hi:[1,0,1]
	ds_read_b128 v[2:5], v88 offset:32
	ds_read_b128 v[6:9], v88 offset:544
	ds_read_b128 v[10:13], v88 offset:1056
	ds_read_b128 v[14:17], v88 offset:1568
	ds_read_b128 v[18:21], v88 offset:2080
	ds_read_b128 v[26:29], v88 offset:2592
	ds_read_b128 v[30:33], v88 offset:3104
	ds_read_b128 v[34:37], v88 offset:3616
	ds_read_b128 v[50:53], v88 offset:4128
	s_waitcnt vmcnt(6) lgkmcnt(8)
	v_pk_fma_f32 v[74:75], v[68:69], v[2:3], v[74:75] op_sel_hi:[1,0,1]
	v_pk_fma_f32 v[76:77], v[66:67], v[2:3], v[78:79] op_sel_hi:[1,0,1]
	s_waitcnt lgkmcnt(7)
	v_pk_fma_f32 v[78:79], v[68:69], v[6:7], v[80:81] op_sel_hi:[1,0,1]
	v_pk_fma_f32 v[80:81], v[66:67], v[6:7], v[82:83] op_sel_hi:[1,0,1]
	s_waitcnt lgkmcnt(6)
	v_pk_fma_f32 v[82:83], v[68:69], v[10:11], v[84:85] op_sel_hi:[1,0,1]
	v_pk_fma_f32 v[84:85], v[66:67], v[10:11], v[100:101] op_sel_hi:[1,0,1]
	s_waitcnt lgkmcnt(5)
	v_pk_fma_f32 v[90:91], v[68:69], v[14:15], v[90:91] op_sel_hi:[1,0,1]
	v_pk_fma_f32 v[100:101], v[66:67], v[14:15], v[102:103] op_sel_hi:[1,0,1]
	s_waitcnt lgkmcnt(4)
	v_pk_fma_f32 v[92:93], v[68:69], v[18:19], v[92:93] op_sel_hi:[1,0,1]
	v_pk_fma_f32 v[102:103], v[66:67], v[18:19], v[104:105] op_sel_hi:[1,0,1]
	s_waitcnt lgkmcnt(3)
	v_pk_fma_f32 v[94:95], v[68:69], v[26:27], v[94:95] op_sel_hi:[1,0,1]
	v_pk_fma_f32 v[104:105], v[66:67], v[26:27], v[106:107] op_sel_hi:[1,0,1]
	s_waitcnt lgkmcnt(2)
	v_pk_fma_f32 v[96:97], v[68:69], v[30:31], v[96:97] op_sel_hi:[1,0,1]
	v_pk_fma_f32 v[106:107], v[66:67], v[30:31], v[108:109] op_sel_hi:[1,0,1]
	s_waitcnt lgkmcnt(1)
	v_pk_fma_f32 v[98:99], v[68:69], v[34:35], v[98:99] op_sel_hi:[1,0,1]
	v_pk_fma_f32 v[108:109], v[66:67], v[34:35], v[110:111] op_sel_hi:[1,0,1]
	s_waitcnt lgkmcnt(0)
	v_pk_fma_f32 v[68:69], v[68:69], v[50:51], v[72:73] op_sel_hi:[1,0,1]
	v_pk_fma_f32 v[66:67], v[66:67], v[50:51], v[70:71] op_sel_hi:[1,0,1]
	s_waitcnt vmcnt(5)
	v_pk_fma_f32 v[70:71], v[64:65], v[2:3], v[74:75] op_sel:[0,1,0]
	v_pk_fma_f32 v[2:3], v[62:63], v[2:3], v[76:77] op_sel:[0,1,0]
	v_pk_fma_f32 v[72:73], v[64:65], v[6:7], v[78:79] op_sel:[0,1,0]
	v_pk_fma_f32 v[6:7], v[62:63], v[6:7], v[80:81] op_sel:[0,1,0]
	v_pk_fma_f32 v[74:75], v[64:65], v[10:11], v[82:83] op_sel:[0,1,0]
	v_pk_fma_f32 v[10:11], v[62:63], v[10:11], v[84:85] op_sel:[0,1,0]
	v_pk_fma_f32 v[76:77], v[64:65], v[14:15], v[90:91] op_sel:[0,1,0]
	v_pk_fma_f32 v[14:15], v[62:63], v[14:15], v[100:101] op_sel:[0,1,0]
	v_pk_fma_f32 v[78:79], v[64:65], v[18:19], v[92:93] op_sel:[0,1,0]
	v_pk_fma_f32 v[18:19], v[62:63], v[18:19], v[102:103] op_sel:[0,1,0]
	v_pk_fma_f32 v[80:81], v[64:65], v[26:27], v[94:95] op_sel:[0,1,0]
	v_pk_fma_f32 v[26:27], v[62:63], v[26:27], v[104:105] op_sel:[0,1,0]
	v_pk_fma_f32 v[82:83], v[64:65], v[30:31], v[96:97] op_sel:[0,1,0]
	v_pk_fma_f32 v[30:31], v[62:63], v[30:31], v[106:107] op_sel:[0,1,0]
	v_pk_fma_f32 v[84:85], v[64:65], v[34:35], v[98:99] op_sel:[0,1,0]
	v_pk_fma_f32 v[34:35], v[62:63], v[34:35], v[108:109] op_sel:[0,1,0]
	v_pk_fma_f32 v[64:65], v[64:65], v[50:51], v[68:69] op_sel:[0,1,0]
	v_pk_fma_f32 v[50:51], v[62:63], v[50:51], v[66:67] op_sel:[0,1,0]
	s_waitcnt vmcnt(4)
; __device__ __forceinline__ void ada_unit(KP Pk, Frame& F, int u) {
;     ...
; #pragma unroll
;         for (int q = 0; q < 16; ++q) {
; #pragma unroll
;             for (int r = 0; r < 9; ++r) a[r] += w[q] * sc[r * 128 + kh * 64 + k0 + q];
;             if ((q & 3) == 3) __builtin_amdgcn_sched_barrier(0); }
	v_pk_fma_f32 v[62:63], v[60:61], v[4:5], v[70:71] op_sel_hi:[1,0,1]
	v_pk_fma_f32 v[2:3], v[58:59], v[4:5], v[2:3] op_sel_hi:[1,0,1]
	v_mov_b32_e32 v4, v5
	v_pk_fma_f32 v[66:67], v[60:61], v[8:9], v[72:73] op_sel_hi:[1,0,1]
	v_pk_fma_f32 v[6:7], v[58:59], v[8:9], v[6:7] op_sel_hi:[1,0,1]
	v_pk_fma_f32 v[10:11], v[58:59], v[12:13], v[10:11] op_sel_hi:[1,0,1]
	v_pk_fma_f32 v[14:15], v[58:59], v[16:17], v[14:15] op_sel_hi:[1,0,1]
	v_pk_fma_f32 v[18:19], v[58:59], v[20:21], v[18:19] op_sel_hi:[1,0,1]
	v_pk_fma_f32 v[26:27], v[58:59], v[28:29], v[26:27] op_sel_hi:[1,0,1]
	v_pk_fma_f32 v[30:31], v[58:59], v[32:33], v[30:31] op_sel_hi:[1,0,1]
	v_pk_fma_f32 v[34:35], v[58:59], v[36:37], v[34:35] op_sel_hi:[1,0,1]
	v_pk_fma_f32 v[50:51], v[58:59], v[52:53], v[50:51] op_sel_hi:[1,0,1]
	s_waitcnt vmcnt(3)
	v_pk_fma_f32 v[58:59], v[56:57], v[4:5], v[62:63] op_sel_hi:[1,0,1]
	v_pk_fma_f32 v[62:63], v[54:55], v[4:5], v[2:3] op_sel_hi:[1,0,1]
	v_mov_b32_e32 v2, v9
	v_pk_fma_f32 v[68:69], v[60:61], v[12:13], v[74:75] op_sel_hi:[1,0,1]
	v_pk_fma_f32 v[70:71], v[60:61], v[16:17], v[76:77] op_sel_hi:[1,0,1]
	v_pk_fma_f32 v[72:73], v[60:61], v[20:21], v[78:79] op_sel_hi:[1,0,1]
	v_pk_fma_f32 v[74:75], v[60:61], v[28:29], v[80:81] op_sel_hi:[1,0,1]
	v_pk_fma_f32 v[76:77], v[60:61], v[32:33], v[82:83] op_sel_hi:[1,0,1]
	v_pk_fma_f32 v[78:79], v[60:61], v[36:37], v[84:85] op_sel_hi:[1,0,1]
	v_pk_fma_f32 v[60:61], v[60:61], v[52:53], v[64:65] op_sel_hi:[1,0,1]
	v_pk_fma_f32 v[64:65], v[56:57], v[2:3], v[66:67] op_sel_hi:[1,0,1]
	v_pk_fma_f32 v[66:67], v[54:55], v[2:3], v[6:7] op_sel_hi:[1,0,1]
	v_mov_b32_e32 v2, v13
	v_pk_fma_f32 v[68:69], v[56:57], v[2:3], v[68:69] op_sel_hi:[1,0,1]
	v_pk_fma_f32 v[80:81], v[54:55], v[2:3], v[10:11] op_sel_hi:[1,0,1]
	v_mov_b32_e32 v2, v17
	v_pk_fma_f32 v[70:71], v[56:57], v[2:3], v[70:71] op_sel_hi:[1,0,1]
	v_pk_fma_f32 v[82:83], v[54:55], v[2:3], v[14:15] op_sel_hi:[1,0,1]
	v_mov_b32_e32 v2, v21
	v_pk_fma_f32 v[72:73], v[56:57], v[2:3], v[72:73] op_sel_hi:[1,0,1]
	v_pk_fma_f32 v[84:85], v[54:55], v[2:3], v[18:19] op_sel_hi:[1,0,1]
	v_mov_b32_e32 v2, v29
	v_pk_fma_f32 v[28:29], v[56:57], v[2:3], v[74:75] op_sel_hi:[1,0,1]
	v_pk_fma_f32 v[26:27], v[54:55], v[2:3], v[26:27] op_sel_hi:[1,0,1]
	v_mov_b32_e32 v2, v33
	v_pk_fma_f32 v[32:33], v[56:57], v[2:3], v[76:77] op_sel_hi:[1,0,1]
	v_pk_fma_f32 v[30:31], v[54:55], v[2:3], v[30:31] op_sel_hi:[1,0,1]
	v_mov_b32_e32 v2, v37
	v_pk_fma_f32 v[36:37], v[56:57], v[2:3], v[78:79] op_sel_hi:[1,0,1]
	v_pk_fma_f32 v[34:35], v[54:55], v[2:3], v[34:35] op_sel_hi:[1,0,1]
	v_mov_b32_e32 v2, v53
	v_pk_fma_f32 v[50:51], v[54:55], v[2:3], v[50:51] op_sel_hi:[1,0,1]
	v_pk_fma_f32 v[74:75], v[56:57], v[2:3], v[60:61] op_sel_hi:[1,0,1]
	ds_read_b128 v[2:5], v88 offset:48
	ds_read_b128 v[6:9], v88 offset:560
	ds_read_b128 v[10:13], v88 offset:1072
	ds_read_b128 v[14:17], v88 offset:1584
	ds_read_b128 v[18:21], v88 offset:2096
	s_waitcnt vmcnt(2) lgkmcnt(4)
	v_pk_fma_f32 v[76:77], v[48:49], v[2:3], v[58:59] op_sel_hi:[1,0,1]
	v_pk_fma_f32 v[78:79], v[46:47], v[2:3], v[62:63] op_sel_hi:[1,0,1]
	s_waitcnt lgkmcnt(3)
	v_pk_fma_f32 v[90:91], v[48:49], v[6:7], v[64:65] op_sel_hi:[1,0,1]
	v_pk_fma_f32 v[92:93], v[46:47], v[6:7], v[66:67] op_sel_hi:[1,0,1]
	ds_read_b128 v[52:55], v88 offset:2608
	ds_read_b128 v[56:59], v88 offset:3120
	ds_read_b128 v[60:63], v88 offset:3632
	ds_read_b128 v[64:67], v88 offset:4144
	s_waitcnt lgkmcnt(6)
	v_pk_fma_f32 v[68:69], v[48:49], v[10:11], v[68:69] op_sel_hi:[1,0,1]
	v_pk_fma_f32 v[80:81], v[46:47], v[10:11], v[80:81] op_sel_hi:[1,0,1]
	s_waitcnt lgkmcnt(5)
	v_pk_fma_f32 v[70:71], v[48:49], v[14:15], v[70:71] op_sel_hi:[1,0,1]
	v_pk_fma_f32 v[82:83], v[46:47], v[14:15], v[82:83] op_sel_hi:[1,0,1]
	s_waitcnt lgkmcnt(4)
	v_pk_fma_f32 v[72:73], v[48:49], v[18:19], v[72:73] op_sel_hi:[1,0,1]
	v_pk_fma_f32 v[84:85], v[46:47], v[18:19], v[84:85] op_sel_hi:[1,0,1]
	s_waitcnt lgkmcnt(3)
	v_pk_fma_f32 v[26:27], v[46:47], v[52:53], v[26:27] op_sel_hi:[1,0,1]
	s_waitcnt lgkmcnt(2)
	v_pk_fma_f32 v[30:31], v[46:47], v[56:57], v[30:31] op_sel_hi:[1,0,1]
	s_waitcnt lgkmcnt(1)
	v_pk_fma_f32 v[34:35], v[46:47], v[60:61], v[34:35] op_sel_hi:[1,0,1]
	s_waitcnt lgkmcnt(0)
	v_pk_fma_f32 v[46:47], v[46:47], v[64:65], v[50:51] op_sel_hi:[1,0,1]
	s_waitcnt vmcnt(1)
; __device__ __forceinline__ void ada_unit(KP Pk, Frame& F, int u) {
;     ...
; #pragma unroll
;         for (int q = 0; q < 16; ++q) {
; #pragma unroll
;             for (int r = 0; r < 9; ++r) a[r] += w[q] * sc[r * 128 + kh * 64 + k0 + q];
;             if ((q & 3) == 3) __builtin_amdgcn_sched_barrier(0); }
;     }
;     if (kh == 1) {
; #pragma unroll
;         for (int r = 0; r < 9; ++r) red[r * 256 + c4] = a[r]; }
	v_pk_fma_f32 v[50:51], v[44:45], v[2:3], v[76:77] op_sel:[0,1,0]
	v_pk_fma_f32 v[2:3], v[42:43], v[2:3], v[78:79] op_sel:[0,1,0]
	v_pk_fma_f32 v[28:29], v[48:49], v[52:53], v[28:29] op_sel_hi:[1,0,1]
	v_pk_fma_f32 v[32:33], v[48:49], v[56:57], v[32:33] op_sel_hi:[1,0,1]
	v_pk_fma_f32 v[36:37], v[48:49], v[60:61], v[36:37] op_sel_hi:[1,0,1]
	v_pk_fma_f32 v[48:49], v[48:49], v[64:65], v[74:75] op_sel_hi:[1,0,1]
	v_pk_fma_f32 v[74:75], v[44:45], v[6:7], v[90:91] op_sel:[0,1,0]
	v_pk_fma_f32 v[6:7], v[42:43], v[6:7], v[92:93] op_sel:[0,1,0]
	v_pk_fma_f32 v[68:69], v[44:45], v[10:11], v[68:69] op_sel:[0,1,0]
	v_pk_fma_f32 v[10:11], v[42:43], v[10:11], v[80:81] op_sel:[0,1,0]
	v_pk_fma_f32 v[70:71], v[44:45], v[14:15], v[70:71] op_sel:[0,1,0]
	v_pk_fma_f32 v[14:15], v[42:43], v[14:15], v[82:83] op_sel:[0,1,0]
	v_pk_fma_f32 v[72:73], v[44:45], v[18:19], v[72:73] op_sel:[0,1,0]
	v_pk_fma_f32 v[18:19], v[42:43], v[18:19], v[84:85] op_sel:[0,1,0]
	v_pk_fma_f32 v[26:27], v[42:43], v[52:53], v[26:27] op_sel:[0,1,0]
	v_pk_fma_f32 v[30:31], v[42:43], v[56:57], v[30:31] op_sel:[0,1,0]
	v_pk_fma_f32 v[34:35], v[42:43], v[60:61], v[34:35] op_sel:[0,1,0]
	v_pk_fma_f32 v[42:43], v[42:43], v[64:65], v[46:47] op_sel:[0,1,0]
	s_waitcnt vmcnt(0)
	v_pk_fma_f32 v[46:47], v[40:41], v[4:5], v[50:51] op_sel_hi:[1,0,1]
	v_pk_fma_f32 v[2:3], v[38:39], v[4:5], v[2:3] op_sel_hi:[1,0,1]
	v_mov_b32_e32 v4, v5
	v_pk_fma_f32 v[28:29], v[44:45], v[52:53], v[28:29] op_sel:[0,1,0]
	v_pk_fma_f32 v[32:33], v[44:45], v[56:57], v[32:33] op_sel:[0,1,0]
	v_pk_fma_f32 v[36:37], v[44:45], v[60:61], v[36:37] op_sel:[0,1,0]
	v_pk_fma_f32 v[44:45], v[44:45], v[64:65], v[48:49] op_sel:[0,1,0]
	v_pk_fma_f32 v[48:49], v[40:41], v[8:9], v[74:75] op_sel_hi:[1,0,1]
	v_pk_fma_f32 v[6:7], v[38:39], v[8:9], v[6:7] op_sel_hi:[1,0,1]
	v_pk_fma_f32 v[50:51], v[22:23], v[4:5], v[2:3] op_sel_hi:[1,0,1]
	v_mov_b32_e32 v2, v9
	v_pk_fma_f32 v[56:57], v[40:41], v[12:13], v[68:69] op_sel_hi:[1,0,1]
	v_pk_fma_f32 v[10:11], v[38:39], v[12:13], v[10:11] op_sel_hi:[1,0,1]
	v_pk_fma_f32 v[76:77], v[40:41], v[62:63], v[36:37] op_sel_hi:[1,0,1]
	v_pk_fma_f32 v[78:79], v[38:39], v[62:63], v[34:35] op_sel_hi:[1,0,1]
	v_pk_fma_f32 v[36:37], v[24:25], v[2:3], v[48:49] op_sel_hi:[1,0,1]
	v_pk_fma_f32 v[34:35], v[22:23], v[2:3], v[6:7] op_sel_hi:[1,0,1]
	v_mov_b32_e32 v2, v13
	v_pk_fma_f32 v[60:61], v[40:41], v[16:17], v[70:71] op_sel_hi:[1,0,1]
	v_pk_fma_f32 v[14:15], v[38:39], v[16:17], v[14:15] op_sel_hi:[1,0,1]
	v_pk_fma_f32 v[64:65], v[40:41], v[20:21], v[72:73] op_sel_hi:[1,0,1]
	v_pk_fma_f32 v[72:73], v[40:41], v[58:59], v[32:33] op_sel_hi:[1,0,1]
	v_pk_fma_f32 v[74:75], v[38:39], v[58:59], v[30:31] op_sel_hi:[1,0,1]
	v_pk_fma_f32 v[32:33], v[24:25], v[2:3], v[56:57] op_sel_hi:[1,0,1]
	v_pk_fma_f32 v[30:31], v[22:23], v[2:3], v[10:11] op_sel_hi:[1,0,1]
	v_mov_b32_e32 v2, v17
	v_pk_fma_f32 v[18:19], v[38:39], v[20:21], v[18:19] op_sel_hi:[1,0,1]
	v_pk_fma_f32 v[68:69], v[40:41], v[54:55], v[28:29] op_sel_hi:[1,0,1]
	v_pk_fma_f32 v[70:71], v[38:39], v[54:55], v[26:27] op_sel_hi:[1,0,1]
	v_pk_fma_f32 v[28:29], v[24:25], v[2:3], v[60:61] op_sel_hi:[1,0,1]
	v_pk_fma_f32 v[26:27], v[22:23], v[2:3], v[14:15] op_sel_hi:[1,0,1]
	v_mov_b32_e32 v2, v21
	v_pk_fma_f32 v[20:21], v[24:25], v[2:3], v[64:65] op_sel_hi:[1,0,1]
	v_pk_fma_f32 v[18:19], v[22:23], v[2:3], v[18:19] op_sel_hi:[1,0,1]
	v_mov_b32_e32 v2, v55
	v_pk_fma_f32 v[16:17], v[24:25], v[2:3], v[68:69] op_sel_hi:[1,0,1]
	v_pk_fma_f32 v[14:15], v[22:23], v[2:3], v[70:71] op_sel_hi:[1,0,1]
	v_mov_b32_e32 v2, v59
	v_pk_fma_f32 v[12:13], v[24:25], v[2:3], v[72:73] op_sel_hi:[1,0,1]
	v_pk_fma_f32 v[10:11], v[22:23], v[2:3], v[74:75] op_sel_hi:[1,0,1]
	v_mov_b32_e32 v2, v63
	v_pk_fma_f32 v[40:41], v[40:41], v[66:67], v[44:45] op_sel_hi:[1,0,1]
	v_pk_fma_f32 v[38:39], v[38:39], v[66:67], v[42:43] op_sel_hi:[1,0,1]
	v_pk_fma_f32 v[8:9], v[24:25], v[2:3], v[76:77] op_sel_hi:[1,0,1]
	v_pk_fma_f32 v[6:7], v[22:23], v[2:3], v[78:79] op_sel_hi:[1,0,1]
	v_mov_b32_e32 v2, v67
	v_pk_fma_f32 v[52:53], v[24:25], v[4:5], v[46:47] op_sel_hi:[1,0,1]
	v_pk_fma_f32 v[4:5], v[24:25], v[2:3], v[40:41] op_sel_hi:[1,0,1]
	v_pk_fma_f32 v[2:3], v[22:23], v[2:3], v[38:39] op_sel_hi:[1,0,1]
	s_add_i32 s8, s8, 16
	s_add_i32 s9, s9, 64
	s_mov_b64 s[18:19], 0xc0000
	s_cmp_gt_u32 s8, 47
	v_lshl_add_u64 v[86:87], v[86:87], 0, s[18:19]
	s_cbranch_scc0 .LBB0_574
	v_readlane_b32 s8, v253, 6
	v_readlane_b32 s9, v253, 7
	s_andn2_b64 vcc, exec, s[8:9]
	s_cbranch_vccnz .LBB0_577
	v_lshl_add_u32 v22, v1, 4, 0
	ds_write_b128 v22, v[50:53] offset:4608
	ds_write_b128 v22, v[34:37] offset:8704
	ds_write_b128 v22, v[30:33] offset:12800
	ds_write_b128 v22, v[26:29] offset:16896
	ds_write_b128 v22, v[18:21] offset:20992
	ds_write_b128 v22, v[14:17] offset:25088
	ds_write_b128 v22, v[10:13] offset:29184
	ds_write_b128 v22, v[6:9] offset:33280
	ds_write_b128 v22, v[2:5] offset:37376
